# P5/P15 epilogue: the second-pass row loads of tokens 0-9 requested in front of the router-softmax reduction chain instead of behind it
# speedup vs baseline: 1.0103x; 1.0090x over previous
; __device__ __forceinline__ void norm_router_phase(const bf16* x1, const float* g, const float* Wr, unsigned char* XN8, float* AFF, LAS float* WT, int gw, int NGW, int lane, int tid, bool table_ready) {
;     ...
;         ss += __shfl_xor(ss, 16); ss += __shfl_xor(ss, 32);
;         const float rstd = 1.0f / sqrtf(ss * (1.f / DM) + RMS_EPS);
;         float lg[4], mx;
; #pragma unroll
;         for (int r = 0; r < 4; ++r) lg[r] = (acc0[r] + acc1[r]) * rstd;
;         mx = fmaxf(fmaxf(lg[0], lg[1]), fmaxf(lg[2], lg[3])); mx = fmaxf(mx, __shfl_xor(mx, 16)); mx = fmaxf(mx, __shfl_xor(mx, 32));
;         float ex[4], sm = 0.f;
; #pragma unroll
;         for (int r = 0; r < 4; ++r) { ex[r] = __builtin_amdgcn_exp2f((lg[r] - mx) * LOG2E); sm += ex[r]; }
;         sm += __shfl_xor(sm, 16); sm += __shfl_xor(sm, 32);
;         { const int row = row0 + ti; const float inv = 1.0f / sm;
; #pragma unroll
;           for (int r = 0; r < 4; ++r) AFF[((size_t)(4 * kq + r) * NB + (row >> 13)) * SEQ + (row & (SEQ - 1))] = ex[r] * inv; }
;         const unsigned rbits = __float_as_uint(rstd);
;         v4u xa[16], xb[16];
; #pragma unroll
;         for (int i = 0; i < 16; ++i) { const bf16* xr = x1 + (size_t)(row0 + i) * DM + 8 * lane; xa[i] = *(const v4u*)xr; xb[i] = *(const v4u*)(xr + 512); }
.LBB0_543:
	s_mov_b32 s98, s10
	s_ashr_i32 s99, s98, 31
	s_lshl_b64 s[100:101], s[98:99], 11
	v_lshl_add_u64 v[214:215], v[168:169], 0, s[100:101]
	global_load_dwordx4 v[188:191], v[214:215], off
	global_load_dwordx4 v[192:195], v[214:215], off offset:1024
	s_or_b32 s98, s10, 1
	s_ashr_i32 s99, s98, 31
	s_lshl_b64 s[100:101], s[98:99], 11
	v_lshl_add_u64 v[214:215], v[168:169], 0, s[100:101]
	global_load_dwordx4 v[196:199], v[214:215], off
	global_load_dwordx4 v[200:203], v[214:215], off offset:1024
	s_or_b32 s98, s10, 2
	s_ashr_i32 s99, s98, 31
	s_lshl_b64 s[100:101], s[98:99], 11
	v_lshl_add_u64 v[214:215], v[168:169], 0, s[100:101]
	global_load_dwordx4 v[158:161], v[214:215], off
	global_load_dwordx4 v[154:157], v[214:215], off offset:1024
	s_or_b32 s98, s10, 3
	s_ashr_i32 s99, s98, 31
	s_lshl_b64 s[100:101], s[98:99], 11
	v_lshl_add_u64 v[214:215], v[168:169], 0, s[100:101]
	global_load_dwordx4 v[150:153], v[214:215], off
	global_load_dwordx4 v[146:149], v[214:215], off offset:1024
	s_or_b32 s98, s10, 4
	s_ashr_i32 s99, s98, 31
	s_lshl_b64 s[100:101], s[98:99], 11
	v_lshl_add_u64 v[214:215], v[168:169], 0, s[100:101]
	global_load_dwordx4 v[142:145], v[214:215], off
	global_load_dwordx4 v[138:141], v[214:215], off offset:1024
	s_or_b32 s98, s10, 5
	s_ashr_i32 s99, s98, 31
	s_lshl_b64 s[100:101], s[98:99], 11
	v_lshl_add_u64 v[214:215], v[168:169], 0, s[100:101]
	global_load_dwordx4 v[134:137], v[214:215], off
	global_load_dwordx4 v[130:133], v[214:215], off offset:1024
	s_or_b32 s98, s10, 6
	s_ashr_i32 s99, s98, 31
	s_lshl_b64 s[100:101], s[98:99], 11
	v_lshl_add_u64 v[214:215], v[168:169], 0, s[100:101]
	global_load_dwordx4 v[126:129], v[214:215], off
	global_load_dwordx4 v[122:125], v[214:215], off offset:1024
	s_or_b32 s98, s10, 7
	s_ashr_i32 s99, s98, 31
	s_lshl_b64 s[100:101], s[98:99], 11
	v_lshl_add_u64 v[214:215], v[168:169], 0, s[100:101]
	global_load_dwordx4 v[118:121], v[214:215], off
	global_load_dwordx4 v[114:117], v[214:215], off offset:1024
	s_or_b32 s98, s10, 8
	s_ashr_i32 s99, s98, 31
	s_lshl_b64 s[100:101], s[98:99], 11
	v_lshl_add_u64 v[214:215], v[168:169], 0, s[100:101]
	global_load_dwordx4 v[110:113], v[214:215], off
	global_load_dwordx4 v[106:109], v[214:215], off offset:1024
	s_or_b32 s98, s10, 9
	s_ashr_i32 s99, s98, 31
	s_lshl_b64 s[100:101], s[98:99], 11
	v_lshl_add_u64 v[214:215], v[168:169], 0, s[100:101]
	global_load_dwordx4 v[102:105], v[214:215], off
	global_load_dwordx4 v[98:101], v[214:215], off offset:1024
	ds_bpermute_b32 v50, v183, v91
	s_mov_b32 s2, 0xf800000
	v_add_f32_e32 v52, v82, v86
	v_add_f32_e32 v53, v83, v87
	s_ashr_i32 s11, s10, 31
	s_waitcnt lgkmcnt(0)
	v_add_f32_e32 v50, v91, v50
	ds_bpermute_b32 v51, v184, v50
	s_or_b32 s34, s10, 1
	s_ashr_i32 s35, s34, 31
	s_or_b32 s30, s10, 2
	s_ashr_i32 s31, s30, 31
	s_waitcnt lgkmcnt(0)
	v_add_f32_e32 v50, v50, v51
	v_fmamk_f32 v50, v50, 0x3a800000, v185
	v_mul_f32_e32 v51, 0x4f800000, v50
	v_cmp_gt_f32_e32 vcc, s2, v50
	s_or_b32 s28, s10, 3
	s_ashr_i32 s29, s28, 31
	v_cndmask_b32_e32 v50, v50, v51, vcc
	v_sqrt_f32_e32 v51, v50
	s_or_b32 s26, s10, 4
	s_ashr_i32 s27, s26, 31
	s_or_b32 s24, s10, 5
	v_add_u32_e32 v54, -1, v51
	v_add_u32_e32 v55, 1, v51
	v_fma_f32 v56, -v54, v51, v50
	v_fma_f32 v57, -v55, v51, v50
	v_cmp_ge_f32_e64 s[4:5], 0, v56
	s_ashr_i32 s25, s24, 31
	s_or_b32 s22, s10, 6
	v_cndmask_b32_e64 v51, v51, v54, s[4:5]
	v_cmp_lt_f32_e64 s[4:5], 0, v57
	s_ashr_i32 s23, s22, 31
	s_or_b32 s20, s10, 7
	v_cndmask_b32_e64 v51, v51, v55, s[4:5]
	v_mul_f32_e32 v54, 0x37800000, v51
	v_cndmask_b32_e32 v51, v51, v54, vcc
	v_cmp_class_f32_e32 vcc, v50, v186
	v_add_f32_e32 v55, v84, v88
	v_readlane_b32 s4, v255, 13
	v_cndmask_b32_e32 v50, v51, v50, vcc
	v_div_scale_f32 v51, s[2:3], v50, v50, 1.0
	v_rcp_f32_e32 v54, v51
	v_div_scale_f32 v56, vcc, 1.0, v50, 1.0
	v_readlane_b32 s5, v255, 14
	v_fma_f32 v57, -v51, v54, 1.0
	v_fmac_f32_e32 v54, v57, v54
	v_mul_f32_e32 v57, v56, v54
	v_fma_f32 v58, -v51, v57, v56
	v_fmac_f32_e32 v57, v58, v54
	v_fma_f32 v51, -v51, v57, v56
	v_div_fmas_f32 v51, v51, v54, v57
	v_div_fixup_f32 v181, v51, v50, 1.0
	v_add_f32_e32 v56, v85, v89
	v_mul_f32_e32 v54, v55, v181
	v_mul_f32_e32 v57, v56, v181
	v_mul_f32_e32 v50, v52, v181
	v_mul_f32_e32 v51, v53, v181
	v_max_f32_e32 v54, v54, v57
	v_max3_f32 v50, v50, v51, v54
	ds_bpermute_b32 v51, v183, v50
	s_ashr_i32 s2, s37, 9
	s_ashr_i32 s3, s2, 31
	v_readlane_b32 s33, v181, 0
	s_ashr_i32 s21, s20, 31
	s_waitcnt lgkmcnt(0)
	v_max_f32_e32 v51, v51, v51
	v_max_f32_e32 v50, v50, v51
	ds_bpermute_b32 v51, v184, v50
	v_mul_f32_e32 v206, s33, v2
	v_mul_f32_e32 v210, s33, v10
	s_or_b32 s18, s10, 8
	s_ashr_i32 s19, s18, 31
	s_waitcnt lgkmcnt(0)
	v_max_f32_e32 v51, v51, v51
	v_max_f32_e32 v50, v50, v51
	v_fma_f32 v51, v52, v181, -v50
	v_fma_f32 v52, v53, v181, -v50
	v_mul_f32_e32 v51, 0x3fb8aa3b, v51
	v_fma_f32 v53, v55, v181, -v50
	v_mul_f32_e32 v52, 0x3fb8aa3b, v52
	v_exp_f32_e32 v54, v51
	v_mul_f32_e32 v53, 0x3fb8aa3b, v53
	v_exp_f32_e32 v55, v52
	v_fma_f32 v50, v56, v181, -v50
	v_exp_f32_e32 v57, v53
	v_mul_f32_e32 v50, 0x3fb8aa3b, v50
	v_exp_f32_e32 v56, v50
	v_add_f32_e32 v50, 0, v54
	v_add_f32_e32 v50, v55, v50
	v_add_f32_e32 v50, v57, v50
	v_add_f32_e32 v50, v56, v50
	ds_bpermute_b32 v51, v183, v50
	s_or_b32 s16, s10, 9
	s_ashr_i32 s17, s16, 31
	s_or_b32 s14, s10, 10
	s_ashr_i32 s15, s14, 31
	s_waitcnt lgkmcnt(0)
	v_add_f32_e32 v52, v50, v51
	ds_bpermute_b32 v53, v184, v52
	v_and_b32_e32 v50, 0x1fff, v90
	v_lshlrev_b32_e32 v162, 2, v50
	v_lshl_add_u64 v[50:51], s[4:5], 0, v[162:163]
	s_or_b32 s12, s10, 11
	s_waitcnt lgkmcnt(0)
; __device__ __forceinline__ unsigned pk4_fp8(float a, float b, float c, float d) { unsigned w = 0u; w = __builtin_amdgcn_cvt_pk_fp8_f32(a, b, w, false); w = __builtin_amdgcn_cvt_pk_fp8_f32(c, d, w, true); return w; }
; __device__ __forceinline__ void unpack8(const v4u w, float (&y)[8]) { y[0] = bf_lo(w.x); y[1] = bf_hi(w.x); y[2] = bf_lo(w.y); y[3] = bf_hi(w.y); y[4] = bf_lo(w.z); y[5] = bf_hi(w.z); y[6] = bf_lo(w.w); y[7] = bf_hi(w.w); }
; __device__ __forceinline__ void norm_router_phase(const bf16* x1, const float* g, const float* Wr, unsigned char* XN8, float* AFF, LAS float* WT, int gw, int NGW, int lane, int tid, bool table_ready) {
;     ...
;         { const int row = row0 + ti; const float inv = 1.0f / sm;
; #pragma unroll
;           for (int r = 0; r < 4; ++r) AFF[((size_t)(4 * kq + r) * NB + (row >> 13)) * SEQ + (row & (SEQ - 1))] = ex[r] * inv; }
;         const unsigned rbits = __float_as_uint(rstd);
;         v4u xa[16], xb[16];
; #pragma unroll
;         for (int i = 0; i < 16; ++i) { const bf16* xr = x1 + (size_t)(row0 + i) * DM + 8 * lane; xa[i] = *(const v4u*)xr; xb[i] = *(const v4u*)(xr + 512); }
; #pragma unroll
;         for (int i = 0; i < 16; ++i) {
;             const float rs = __uint_as_float((unsigned)__builtin_amdgcn_readlane((int)rbits, i));
;             float v[16]; { float t[8]; unpack8(xa[i], t);
; #pragma unroll
;                 for (int j = 0; j < 8; ++j) v[j] = t[j] * (rs * gg[j]);
;                 unpack8(xb[i], t);
; #pragma unroll
;                 for (int j = 0; j < 8; ++j) v[8 + j] = t[j] * (rs * gg[8 + j]); }
;             unsigned char* o = XN8 + (size_t)(row0 + i) * DM + 8 * lane;
;             *(v2u*)o = (v2u){pg8::pk4_fp8(v[0], v[1], v[2], v[3]), pg8::pk4_fp8(v[4], v[5], v[6], v[7])};
;             *(v2u*)(o + 512) = (v2u){pg8::pk4_fp8(v[8], v[9], v[10], v[11]), pg8::pk4_fp8(v[12], v[13], v[14], v[15])};
	v_add_f32_e32 v58, v52, v53
	v_div_scale_f32 v59, s[4:5], v58, v58, 1.0
	v_rcp_f32_e32 v60, v59
	v_div_scale_f32 v61, vcc, 1.0, v58, 1.0
	v_lshl_add_u64 v[52:53], s[2:3], 0, v[164:165]
	v_fma_f32 v62, -v59, v60, 1.0
	v_fmac_f32_e32 v60, v62, v60
	v_mul_f32_e32 v62, v61, v60
	v_fma_f32 v63, -v59, v62, v61
	v_fmac_f32_e32 v62, v63, v60
	v_fma_f32 v59, -v59, v62, v61
	v_div_fmas_f32 v59, v59, v60, v62
	v_div_fixup_f32 v58, v59, v58, 1.0
	v_lshlrev_b64 v[52:53], 15, v[52:53]
	v_mul_f32_e32 v54, v54, v58
	v_lshl_add_u64 v[52:53], v[50:51], 0, v[52:53]
	global_store_dword v[52:53], v54, off
	v_lshl_add_u64 v[52:53], s[2:3], 0, v[172:173]
	v_lshlrev_b64 v[52:53], 15, v[52:53]
	v_mul_f32_e32 v54, v55, v58
	v_lshl_add_u64 v[52:53], v[50:51], 0, v[52:53]
	global_store_dword v[52:53], v54, off
	v_lshl_add_u64 v[52:53], s[2:3], 0, v[174:175]
	v_lshlrev_b64 v[52:53], 15, v[52:53]
	v_mul_f32_e32 v54, v57, v58
	v_lshl_add_u64 v[52:53], v[50:51], 0, v[52:53]
	global_store_dword v[52:53], v54, off
	v_lshl_add_u64 v[52:53], s[2:3], 0, v[176:177]
	v_lshlrev_b64 v[52:53], 15, v[52:53]
	v_mul_f32_e32 v54, v56, v58
	v_lshl_add_u64 v[50:51], v[50:51], 0, v[52:53]
	s_lshl_b64 s[2:3], s[10:11], 11
	global_store_dword v[50:51], v54, off
	v_lshl_add_u64 v[50:51], v[168:169], 0, s[2:3]
	s_nop 0
	s_nop 0
	s_lshl_b64 s[2:3], s[34:35], 11
	v_lshl_add_u64 v[50:51], v[168:169], 0, s[2:3]
	s_nop 0
	s_nop 0
	s_lshl_b64 s[2:3], s[30:31], 11
	v_lshl_add_u64 v[50:51], v[168:169], 0, s[2:3]
	s_nop 0
	s_nop 0
	s_lshl_b64 s[2:3], s[28:29], 11
	v_lshl_add_u64 v[50:51], v[168:169], 0, s[2:3]
	s_nop 0
	s_nop 0
	s_lshl_b64 s[2:3], s[26:27], 11
	v_lshl_add_u64 v[50:51], v[168:169], 0, s[2:3]
	s_lshl_b64 s[2:3], s[24:25], 11
	s_nop 0
	s_nop 0
	v_lshl_add_u64 v[50:51], v[168:169], 0, s[2:3]
	s_lshl_b64 s[2:3], s[22:23], 11
	s_nop 0
	s_nop 0
	v_lshl_add_u64 v[50:51], v[168:169], 0, s[2:3]
	s_lshl_b64 s[2:3], s[20:21], 11
	s_nop 0
	s_nop 0
	v_lshl_add_u64 v[50:51], v[168:169], 0, s[2:3]
	s_lshl_b64 s[2:3], s[18:19], 11
	s_nop 0
	s_nop 0
	v_lshl_add_u64 v[50:51], v[168:169], 0, s[2:3]
	s_lshl_b64 s[2:3], s[16:17], 11
	s_nop 0
	s_nop 0
	v_lshl_add_u64 v[50:51], v[168:169], 0, s[2:3]
	s_lshl_b64 s[2:3], s[14:15], 11
	s_ashr_i32 s13, s12, 31
	s_or_b32 s8, s10, 12
	s_nop 0
	s_nop 0
	v_lshl_add_u64 v[50:51], v[168:169], 0, s[2:3]
	s_lshl_b64 s[2:3], s[12:13], 11
	s_ashr_i32 s9, s8, 31
	s_or_b32 s6, s10, 13
	global_load_dwordx4 v[94:97], v[50:51], off
	global_load_dwordx4 v[90:93], v[50:51], off offset:1024
	v_lshl_add_u64 v[50:51], v[168:169], 0, s[2:3]
	s_lshl_b64 s[2:3], s[8:9], 11
	s_ashr_i32 s7, s6, 31
	s_or_b32 s4, s10, 14
	global_load_dwordx4 v[86:89], v[50:51], off
	global_load_dwordx4 v[82:85], v[50:51], off offset:1024
	v_lshl_add_u64 v[50:51], v[168:169], 0, s[2:3]
	s_lshl_b64 s[2:3], s[6:7], 11
	s_ashr_i32 s5, s4, 31
	global_load_dwordx4 v[78:81], v[50:51], off
	global_load_dwordx4 v[74:77], v[50:51], off offset:1024
	v_lshl_add_u64 v[50:51], v[168:169], 0, s[2:3]
	s_lshl_b64 s[2:3], s[4:5], 11
	global_load_dwordx4 v[70:73], v[50:51], off
	global_load_dwordx4 v[66:69], v[50:51], off offset:1024
	v_lshl_add_u64 v[50:51], v[168:169], 0, s[2:3]
	s_or_b32 s2, s10, 15
	s_lshl_b64 s[10:11], s[10:11], 10
	s_ashr_i32 s3, s2, 31
	s_lshl_b64 s[38:39], s[2:3], 11
	global_load_dwordx4 v[62:65], v[50:51], off
	global_load_dwordx4 v[58:61], v[50:51], off offset:1024
	v_lshl_add_u64 v[50:51], v[168:169], 0, s[38:39]
	global_load_dwordx4 v[54:57], v[50:51], off
	s_nop 0
	global_load_dwordx4 v[50:53], v[50:51], off offset:1024
	s_lshl_b64 s[8:9], s[8:9], 10
	s_lshl_b64 s[6:7], s[6:7], 10
	s_lshl_b64 s[4:5], s[4:5], 10
	s_lshl_b64 s[2:3], s[2:3], 10
	v_add_u32_e32 v180, s36, v180
	s_waitcnt vmcnt(31)
	v_lshlrev_b32_e32 v162, 16, v188
	v_and_b32_e32 v187, 0xffff0000, v188
	v_mul_f32_e32 v162, v206, v162
	v_mul_f32_e32 v206, s33, v3
	v_lshlrev_b32_e32 v188, 16, v189
	v_mul_f32_e32 v187, v206, v187
	v_mul_f32_e32 v206, s33, v4
	v_and_b32_e32 v189, 0xffff0000, v189
	v_mul_f32_e32 v206, v206, v188
	v_mul_f32_e32 v188, s33, v5
	v_lshlrev_b32_e32 v204, 16, v190
	v_mul_f32_e32 v207, v188, v189
	v_mul_f32_e32 v188, s33, v6
	v_and_b32_e32 v190, 0xffff0000, v190
	v_mul_f32_e32 v204, v188, v204
	v_mul_f32_e32 v188, s33, v7
	v_lshlrev_b32_e32 v205, 16, v191
	v_mul_f32_e32 v190, v188, v190
	v_mul_f32_e32 v188, s33, v8
	v_and_b32_e32 v191, 0xffff0000, v191
	v_mul_f32_e32 v205, v188, v205
	v_mul_f32_e32 v188, s33, v9
	v_mul_f32_e32 v208, v188, v191
	s_waitcnt vmcnt(30)
	v_lshlrev_b32_e32 v188, 16, v192
	v_and_b32_e32 v189, 0xffff0000, v192
	v_mul_f32_e32 v210, v210, v188
	v_mul_f32_e32 v188, s33, v11
	v_lshlrev_b32_e32 v191, 16, v193
	v_mul_f32_e32 v211, v188, v189
	v_mul_f32_e32 v188, s33, v12
	v_and_b32_e32 v192, 0xffff0000, v193
	v_mul_f32_e32 v212, v188, v191
	v_mul_f32_e32 v188, s33, v13
	v_lshlrev_b32_e32 v193, 16, v194
	v_mul_f32_e32 v192, v188, v192
	v_mul_f32_e32 v188, s33, v14
	v_and_b32_e32 v194, 0xffff0000, v194
	v_mul_f32_e32 v193, v188, v193
	v_mul_f32_e32 v188, s33, v15
	v_lshlrev_b32_e32 v209, 16, v195
	v_mul_f32_e32 v194, v188, v194
	v_mul_f32_e32 v188, s33, v16
	v_and_b32_e32 v195, 0xffff0000, v195
	v_mul_f32_e32 v209, v188, v209
	v_mul_f32_e32 v188, s33, v17
	v_mul_f32_e32 v195, v188, v195
	v_mov_b32_e32 v188, v163
	v_mov_b32_e32 v189, v163
	v_cvt_pk_fp8_f32 v188, v162, v187
	v_cvt_pk_fp8_f32 v189, v204, v190
	v_mov_b32_e32 v190, v163
	v_mov_b32_e32 v191, v163
	v_cvt_pk_fp8_f32 v190, v210, v211
	v_cvt_pk_fp8_f32 v191, v193, v194
	v_cvt_pk_fp8_f32 v188, v206, v207 op_sel:[0,0,1]
	v_cvt_pk_fp8_f32 v189, v205, v208 op_sel:[0,0,1]
	v_cvt_pk_fp8_f32 v190, v212, v192 op_sel:[0,0,1]
	v_cvt_pk_fp8_f32 v191, v209, v195 op_sel:[0,0,1]
	v_lshl_add_u64 v[192:193], v[170:171], 0, s[10:11]
	v_readlane_b32 s10, v181, 1
	s_waitcnt vmcnt(29)
; __device__ __forceinline__ unsigned pk4_fp8(float a, float b, float c, float d) { unsigned w = 0u; w = __builtin_amdgcn_cvt_pk_fp8_f32(a, b, w, false); w = __builtin_amdgcn_cvt_pk_fp8_f32(c, d, w, true); return w; }
; __device__ __forceinline__ void unpack8(const v4u w, float (&y)[8]) { y[0] = bf_lo(w.x); y[1] = bf_hi(w.x); y[2] = bf_lo(w.y); y[3] = bf_hi(w.y); y[4] = bf_lo(w.z); y[5] = bf_hi(w.z); y[6] = bf_lo(w.w); y[7] = bf_hi(w.w); }
; __device__ __forceinline__ void norm_router_phase(const bf16* x1, const float* g, const float* Wr, unsigned char* XN8, float* AFF, LAS float* WT, int gw, int NGW, int lane, int tid, bool table_ready) {
;     ...
;         for (int i = 0; i < 16; ++i) {
;             const float rs = __uint_as_float((unsigned)__builtin_amdgcn_readlane((int)rbits, i));
;             float v[16]; { float t[8]; unpack8(xa[i], t);
; #pragma unroll
;                 for (int j = 0; j < 8; ++j) v[j] = t[j] * (rs * gg[j]);
;                 unpack8(xb[i], t);
; #pragma unroll
;                 for (int j = 0; j < 8; ++j) v[8 + j] = t[j] * (rs * gg[8 + j]); }
;             unsigned char* o = XN8 + (size_t)(row0 + i) * DM + 8 * lane;
;             *(v2u*)o = (v2u){pg8::pk4_fp8(v[0], v[1], v[2], v[3]), pg8::pk4_fp8(v[4], v[5], v[6], v[7])};
;             *(v2u*)(o + 512) = (v2u){pg8::pk4_fp8(v[8], v[9], v[10], v[11]), pg8::pk4_fp8(v[12], v[13], v[14], v[15])};
	v_lshlrev_b32_e32 v162, 16, v196
	v_and_b32_e32 v187, 0xffff0000, v196
	v_mul_f32_e32 v194, s10, v2
	v_mul_f32_e32 v162, v194, v162
	v_mul_f32_e32 v194, s10, v3
	global_store_dwordx2 v[192:193], v[188:189], off
	global_store_dwordx2 v[192:193], v[190:191], off offset:512
	v_lshlrev_b32_e32 v188, 16, v197
	v_mul_f32_e32 v187, v194, v187
	v_mul_f32_e32 v194, s10, v4
	v_and_b32_e32 v189, 0xffff0000, v197
	v_mul_f32_e32 v194, v194, v188
	v_mul_f32_e32 v188, s10, v5
	v_lshlrev_b32_e32 v190, 16, v198
	v_mul_f32_e32 v195, v188, v189
	v_mul_f32_e32 v188, s10, v6
	v_and_b32_e32 v191, 0xffff0000, v198
	v_mul_f32_e32 v190, v188, v190
	v_mul_f32_e32 v188, s10, v7
	v_lshlrev_b32_e32 v192, 16, v199
	v_mul_f32_e32 v191, v188, v191
	v_mul_f32_e32 v188, s10, v8
	v_and_b32_e32 v193, 0xffff0000, v199
	v_mul_f32_e32 v192, v188, v192
	v_mul_f32_e32 v188, s10, v9
	v_mul_f32_e32 v193, v188, v193
	s_waitcnt vmcnt(30)
	v_lshlrev_b32_e32 v188, 16, v200
	v_lshlrev_b32_e32 v198, 16, v202
	v_and_b32_e32 v199, 0xffff0000, v202
	v_mul_f32_e32 v202, s10, v10
	v_and_b32_e32 v189, 0xffff0000, v200
	v_mul_f32_e32 v202, v202, v188
	v_mul_f32_e32 v188, s10, v11
	v_lshlrev_b32_e32 v196, 16, v201
	v_and_b32_e32 v197, 0xffff0000, v201
	v_lshlrev_b32_e32 v200, 16, v203
	v_and_b32_e32 v201, 0xffff0000, v203
	v_mul_f32_e32 v203, v188, v189
	v_mul_f32_e32 v188, s10, v12
	v_mul_f32_e32 v196, v188, v196
	v_mul_f32_e32 v188, s10, v13
	v_mul_f32_e32 v197, v188, v197
	v_mul_f32_e32 v188, s10, v14
	v_mul_f32_e32 v198, v188, v198
	v_mul_f32_e32 v188, s10, v15
	v_mul_f32_e32 v199, v188, v199
	v_mul_f32_e32 v188, s10, v16
	v_mul_f32_e32 v200, v188, v200
	v_mul_f32_e32 v188, s10, v17
	v_mul_f32_e32 v201, v188, v201
	v_mov_b32_e32 v188, v163
	v_mov_b32_e32 v189, v163
	v_cvt_pk_fp8_f32 v188, v162, v187
	v_cvt_pk_fp8_f32 v189, v190, v191
	v_mov_b32_e32 v190, v163
	v_mov_b32_e32 v191, v163
	v_cvt_pk_fp8_f32 v190, v202, v203
	v_cvt_pk_fp8_f32 v191, v198, v199
	v_cvt_pk_fp8_f32 v188, v194, v195 op_sel:[0,0,1]
	v_cvt_pk_fp8_f32 v189, v192, v193 op_sel:[0,0,1]
	v_cvt_pk_fp8_f32 v190, v196, v197 op_sel:[0,0,1]
	v_cvt_pk_fp8_f32 v191, v200, v201 op_sel:[0,0,1]
	s_lshl_b64 s[10:11], s[34:35], 10
	v_lshl_add_u64 v[192:193], v[170:171], 0, s[10:11]
	v_readlane_b32 s10, v181, 2
	global_store_dwordx2 v[192:193], v[188:189], off
	global_store_dwordx2 v[192:193], v[190:191], off offset:512
	s_waitcnt vmcnt(31)
	v_lshlrev_b32_e32 v162, 16, v158
	v_mul_f32_e32 v190, s10, v2
	v_and_b32_e32 v158, 0xffff0000, v158
	v_mul_f32_e32 v162, v190, v162
	v_mul_f32_e32 v190, s10, v3
	v_lshlrev_b32_e32 v187, 16, v159
	v_mul_f32_e32 v158, v190, v158
	v_mul_f32_e32 v190, s10, v4
	v_and_b32_e32 v159, 0xffff0000, v159
	v_mul_f32_e32 v187, v190, v187
	v_mul_f32_e32 v190, s10, v5
	v_lshlrev_b32_e32 v188, 16, v160
	v_mul_f32_e32 v159, v190, v159
	v_mul_f32_e32 v190, s10, v6
	v_and_b32_e32 v160, 0xffff0000, v160
	v_mul_f32_e32 v188, v190, v188
	v_mul_f32_e32 v190, s10, v7
	v_lshlrev_b32_e32 v189, 16, v161
	v_mul_f32_e32 v160, v190, v160
	v_mul_f32_e32 v190, s10, v8
	v_and_b32_e32 v161, 0xffff0000, v161
	v_mul_f32_e32 v189, v190, v189
	v_mul_f32_e32 v190, s10, v9
	v_mul_f32_e32 v161, v190, v161
	s_waitcnt vmcnt(30)
	v_lshlrev_b32_e32 v190, 16, v154
	v_mul_f32_e32 v194, s10, v10
	v_and_b32_e32 v154, 0xffff0000, v154
	v_mul_f32_e32 v190, v194, v190
	v_mul_f32_e32 v194, s10, v11
	v_lshlrev_b32_e32 v191, 16, v155
	v_mul_f32_e32 v194, v194, v154
	v_mul_f32_e32 v154, s10, v12
	v_and_b32_e32 v155, 0xffff0000, v155
	v_mul_f32_e32 v191, v154, v191
	v_mul_f32_e32 v154, s10, v13
	v_lshlrev_b32_e32 v192, 16, v156
	v_mul_f32_e32 v195, v154, v155
	v_mul_f32_e32 v154, s10, v14
	v_and_b32_e32 v156, 0xffff0000, v156
	v_mul_f32_e32 v192, v154, v192
	v_mul_f32_e32 v154, s10, v15
	v_lshlrev_b32_e32 v193, 16, v157
	v_mul_f32_e32 v196, v154, v156
	v_mul_f32_e32 v154, s10, v16
	v_and_b32_e32 v157, 0xffff0000, v157
	v_mul_f32_e32 v193, v154, v193
	v_mul_f32_e32 v154, s10, v17
	v_mul_f32_e32 v197, v154, v157
	v_mov_b32_e32 v154, v163
	v_mov_b32_e32 v155, v163
	v_cvt_pk_fp8_f32 v154, v162, v158
	v_cvt_pk_fp8_f32 v155, v188, v160
	v_mov_b32_e32 v156, v163
	v_mov_b32_e32 v157, v163
	v_cvt_pk_fp8_f32 v156, v190, v194
	v_cvt_pk_fp8_f32 v157, v192, v196
	v_cvt_pk_fp8_f32 v154, v187, v159 op_sel:[0,0,1]
	v_cvt_pk_fp8_f32 v155, v189, v161 op_sel:[0,0,1]
	v_cvt_pk_fp8_f32 v156, v191, v195 op_sel:[0,0,1]
	v_cvt_pk_fp8_f32 v157, v193, v197 op_sel:[0,0,1]
	s_lshl_b64 s[10:11], s[30:31], 10
	v_lshl_add_u64 v[158:159], v[170:171], 0, s[10:11]
	v_readlane_b32 s10, v181, 3
	global_store_dwordx2 v[158:159], v[154:155], off
	global_store_dwordx2 v[158:159], v[156:157], off offset:512
	s_waitcnt vmcnt(31)
	v_lshlrev_b32_e32 v154, 16, v150
	v_mul_f32_e32 v158, s10, v2
	v_and_b32_e32 v150, 0xffff0000, v150
	v_mul_f32_e32 v154, v158, v154
	v_mul_f32_e32 v158, s10, v3
	v_lshlrev_b32_e32 v155, 16, v151
	v_mul_f32_e32 v150, v158, v150
	v_mul_f32_e32 v158, s10, v4
	v_and_b32_e32 v151, 0xffff0000, v151
	v_mul_f32_e32 v155, v158, v155
	v_mul_f32_e32 v158, s10, v5
	v_lshlrev_b32_e32 v156, 16, v152
	v_mul_f32_e32 v151, v158, v151
	v_mul_f32_e32 v158, s10, v6
	v_and_b32_e32 v152, 0xffff0000, v152
	v_mul_f32_e32 v156, v158, v156
	v_mul_f32_e32 v158, s10, v7
	v_lshlrev_b32_e32 v157, 16, v153
	v_mul_f32_e32 v152, v158, v152
	v_mul_f32_e32 v158, s10, v8
	v_and_b32_e32 v153, 0xffff0000, v153
	v_mul_f32_e32 v157, v158, v157
	v_mul_f32_e32 v158, s10, v9
	v_mul_f32_e32 v153, v158, v153
	s_waitcnt vmcnt(30)
; __device__ __forceinline__ unsigned pk4_fp8(float a, float b, float c, float d) { unsigned w = 0u; w = __builtin_amdgcn_cvt_pk_fp8_f32(a, b, w, false); w = __builtin_amdgcn_cvt_pk_fp8_f32(c, d, w, true); return w; }
; __device__ __forceinline__ void unpack8(const v4u w, float (&y)[8]) { y[0] = bf_lo(w.x); y[1] = bf_hi(w.x); y[2] = bf_lo(w.y); y[3] = bf_hi(w.y); y[4] = bf_lo(w.z); y[5] = bf_hi(w.z); y[6] = bf_lo(w.w); y[7] = bf_hi(w.w); }
; __device__ __forceinline__ void norm_router_phase(const bf16* x1, const float* g, const float* Wr, unsigned char* XN8, float* AFF, LAS float* WT, int gw, int NGW, int lane, int tid, bool table_ready) {
;     ...
;         for (int i = 0; i < 16; ++i) {
;             const float rs = __uint_as_float((unsigned)__builtin_amdgcn_readlane((int)rbits, i));
;             float v[16]; { float t[8]; unpack8(xa[i], t);
; #pragma unroll
;                 for (int j = 0; j < 8; ++j) v[j] = t[j] * (rs * gg[j]);
;                 unpack8(xb[i], t);
; #pragma unroll
;                 for (int j = 0; j < 8; ++j) v[8 + j] = t[j] * (rs * gg[8 + j]); }
;             unsigned char* o = XN8 + (size_t)(row0 + i) * DM + 8 * lane;
;             *(v2u*)o = (v2u){pg8::pk4_fp8(v[0], v[1], v[2], v[3]), pg8::pk4_fp8(v[4], v[5], v[6], v[7])};
;             *(v2u*)(o + 512) = (v2u){pg8::pk4_fp8(v[8], v[9], v[10], v[11]), pg8::pk4_fp8(v[12], v[13], v[14], v[15])};
	v_lshlrev_b32_e32 v158, 16, v146
	v_mul_f32_e32 v162, s10, v10
	v_and_b32_e32 v146, 0xffff0000, v146
	v_mul_f32_e32 v158, v162, v158
	v_mul_f32_e32 v162, s10, v11
	v_lshlrev_b32_e32 v159, 16, v147
	v_mul_f32_e32 v162, v162, v146
	v_mul_f32_e32 v146, s10, v12
	v_and_b32_e32 v147, 0xffff0000, v147
	v_mul_f32_e32 v159, v146, v159
	v_mul_f32_e32 v146, s10, v13
	v_lshlrev_b32_e32 v160, 16, v148
	v_mul_f32_e32 v187, v146, v147
	v_mul_f32_e32 v146, s10, v14
	v_and_b32_e32 v148, 0xffff0000, v148
	v_mul_f32_e32 v160, v146, v160
	v_mul_f32_e32 v146, s10, v15
	v_lshlrev_b32_e32 v161, 16, v149
	v_mul_f32_e32 v188, v146, v148
	v_mul_f32_e32 v146, s10, v16
	v_and_b32_e32 v149, 0xffff0000, v149
	v_mul_f32_e32 v161, v146, v161
	v_mul_f32_e32 v146, s10, v17
	v_mul_f32_e32 v189, v146, v149
	v_mov_b32_e32 v146, v163
	v_mov_b32_e32 v147, v163
	v_cvt_pk_fp8_f32 v146, v154, v150
	v_cvt_pk_fp8_f32 v147, v156, v152
	v_mov_b32_e32 v148, v163
	v_mov_b32_e32 v149, v163
	v_cvt_pk_fp8_f32 v148, v158, v162
	v_cvt_pk_fp8_f32 v149, v160, v188
	v_cvt_pk_fp8_f32 v146, v155, v151 op_sel:[0,0,1]
	v_cvt_pk_fp8_f32 v147, v157, v153 op_sel:[0,0,1]
	v_cvt_pk_fp8_f32 v148, v159, v187 op_sel:[0,0,1]
	v_cvt_pk_fp8_f32 v149, v161, v189 op_sel:[0,0,1]
	s_lshl_b64 s[10:11], s[28:29], 10
	v_lshl_add_u64 v[150:151], v[170:171], 0, s[10:11]
	v_readlane_b32 s10, v181, 4
	global_store_dwordx2 v[150:151], v[146:147], off
	global_store_dwordx2 v[150:151], v[148:149], off offset:512
	s_waitcnt vmcnt(31)
	v_lshlrev_b32_e32 v146, 16, v142
	v_mul_f32_e32 v150, s10, v2
	v_and_b32_e32 v142, 0xffff0000, v142
	v_mul_f32_e32 v146, v150, v146
	v_mul_f32_e32 v150, s10, v3
	v_lshlrev_b32_e32 v147, 16, v143
	v_mul_f32_e32 v142, v150, v142
	v_mul_f32_e32 v150, s10, v4
	v_and_b32_e32 v143, 0xffff0000, v143
	v_mul_f32_e32 v147, v150, v147
	v_mul_f32_e32 v150, s10, v5
	v_lshlrev_b32_e32 v148, 16, v144
	v_mul_f32_e32 v143, v150, v143
	v_mul_f32_e32 v150, s10, v6
	v_and_b32_e32 v144, 0xffff0000, v144
	v_mul_f32_e32 v148, v150, v148
	v_mul_f32_e32 v150, s10, v7
	v_lshlrev_b32_e32 v149, 16, v145
	v_mul_f32_e32 v144, v150, v144
	v_mul_f32_e32 v150, s10, v8
	v_and_b32_e32 v145, 0xffff0000, v145
	v_mul_f32_e32 v149, v150, v149
	v_mul_f32_e32 v150, s10, v9
	v_mul_f32_e32 v145, v150, v145
	s_waitcnt vmcnt(30)
	v_lshlrev_b32_e32 v150, 16, v138
	v_mul_f32_e32 v154, s10, v10
	v_and_b32_e32 v138, 0xffff0000, v138
	v_mul_f32_e32 v150, v154, v150
	v_mul_f32_e32 v154, s10, v11
	v_lshlrev_b32_e32 v151, 16, v139
	v_mul_f32_e32 v154, v154, v138
	v_mul_f32_e32 v138, s10, v12
	v_and_b32_e32 v139, 0xffff0000, v139
	v_mul_f32_e32 v151, v138, v151
	v_mul_f32_e32 v138, s10, v13
	v_lshlrev_b32_e32 v152, 16, v140
	v_mul_f32_e32 v155, v138, v139
	v_mul_f32_e32 v138, s10, v14
	v_and_b32_e32 v140, 0xffff0000, v140
	v_mul_f32_e32 v152, v138, v152
	v_mul_f32_e32 v138, s10, v15
	v_lshlrev_b32_e32 v153, 16, v141
	v_mul_f32_e32 v156, v138, v140
	v_mul_f32_e32 v138, s10, v16
	v_and_b32_e32 v141, 0xffff0000, v141
	v_mul_f32_e32 v153, v138, v153
	v_mul_f32_e32 v138, s10, v17
	v_mul_f32_e32 v157, v138, v141
	v_mov_b32_e32 v138, v163
	v_mov_b32_e32 v139, v163
	v_cvt_pk_fp8_f32 v138, v146, v142
	v_cvt_pk_fp8_f32 v139, v148, v144
	v_mov_b32_e32 v140, v163
	v_mov_b32_e32 v141, v163
	v_cvt_pk_fp8_f32 v140, v150, v154
	v_cvt_pk_fp8_f32 v141, v152, v156
	v_cvt_pk_fp8_f32 v138, v147, v143 op_sel:[0,0,1]
	v_cvt_pk_fp8_f32 v139, v149, v145 op_sel:[0,0,1]
	v_cvt_pk_fp8_f32 v140, v151, v155 op_sel:[0,0,1]
	v_cvt_pk_fp8_f32 v141, v153, v157 op_sel:[0,0,1]
	s_lshl_b64 s[10:11], s[26:27], 10
	v_lshl_add_u64 v[142:143], v[170:171], 0, s[10:11]
	v_readlane_b32 s10, v181, 5
	global_store_dwordx2 v[142:143], v[138:139], off
	global_store_dwordx2 v[142:143], v[140:141], off offset:512
	s_waitcnt vmcnt(31)
	v_lshlrev_b32_e32 v138, 16, v134
	v_mul_f32_e32 v142, s10, v2
	v_and_b32_e32 v134, 0xffff0000, v134
	v_mul_f32_e32 v138, v142, v138
	v_mul_f32_e32 v142, s10, v3
	v_lshlrev_b32_e32 v139, 16, v135
	v_mul_f32_e32 v134, v142, v134
	v_mul_f32_e32 v142, s10, v4
	v_and_b32_e32 v135, 0xffff0000, v135
	v_mul_f32_e32 v139, v142, v139
	v_mul_f32_e32 v142, s10, v5
	v_lshlrev_b32_e32 v140, 16, v136
	v_mul_f32_e32 v135, v142, v135
	v_mul_f32_e32 v142, s10, v6
	v_and_b32_e32 v136, 0xffff0000, v136
	v_mul_f32_e32 v140, v142, v140
	v_mul_f32_e32 v142, s10, v7
	v_lshlrev_b32_e32 v141, 16, v137
	v_mul_f32_e32 v136, v142, v136
	v_mul_f32_e32 v142, s10, v8
	v_and_b32_e32 v137, 0xffff0000, v137
	v_mul_f32_e32 v141, v142, v141
	v_mul_f32_e32 v142, s10, v9
	v_mul_f32_e32 v137, v142, v137
	s_waitcnt vmcnt(30)
	v_lshlrev_b32_e32 v142, 16, v130
	v_mul_f32_e32 v146, s10, v10
	v_and_b32_e32 v130, 0xffff0000, v130
	v_mul_f32_e32 v142, v146, v142
	v_mul_f32_e32 v146, s10, v11
	v_lshlrev_b32_e32 v143, 16, v131
	v_mul_f32_e32 v146, v146, v130
	v_mul_f32_e32 v130, s10, v12
	v_and_b32_e32 v131, 0xffff0000, v131
	v_mul_f32_e32 v143, v130, v143
	v_mul_f32_e32 v130, s10, v13
	v_lshlrev_b32_e32 v144, 16, v132
	v_mul_f32_e32 v147, v130, v131
	v_mul_f32_e32 v130, s10, v14
	v_and_b32_e32 v132, 0xffff0000, v132
	v_mul_f32_e32 v144, v130, v144
	v_mul_f32_e32 v130, s10, v15
	v_lshlrev_b32_e32 v145, 16, v133
	v_mul_f32_e32 v148, v130, v132
	v_mul_f32_e32 v130, s10, v16
	v_and_b32_e32 v133, 0xffff0000, v133
	v_mul_f32_e32 v145, v130, v145
	v_mul_f32_e32 v130, s10, v17
	v_mul_f32_e32 v149, v130, v133
	v_mov_b32_e32 v130, v163
	v_mov_b32_e32 v131, v163
	v_cvt_pk_fp8_f32 v130, v138, v134
	v_cvt_pk_fp8_f32 v131, v140, v136
	v_mov_b32_e32 v132, v163
	v_mov_b32_e32 v133, v163
	v_cvt_pk_fp8_f32 v132, v142, v146
	v_cvt_pk_fp8_f32 v133, v144, v148
	v_cvt_pk_fp8_f32 v130, v139, v135 op_sel:[0,0,1]
	v_cvt_pk_fp8_f32 v131, v141, v137 op_sel:[0,0,1]
	v_cvt_pk_fp8_f32 v132, v143, v147 op_sel:[0,0,1]
	v_cvt_pk_fp8_f32 v133, v145, v149 op_sel:[0,0,1]
	s_lshl_b64 s[10:11], s[24:25], 10
	v_lshl_add_u64 v[134:135], v[170:171], 0, s[10:11]
	v_readlane_b32 s10, v181, 6
	global_store_dwordx2 v[134:135], v[130:131], off
	global_store_dwordx2 v[134:135], v[132:133], off offset:512
	s_waitcnt vmcnt(31)
; __device__ __forceinline__ unsigned pk4_fp8(float a, float b, float c, float d) { unsigned w = 0u; w = __builtin_amdgcn_cvt_pk_fp8_f32(a, b, w, false); w = __builtin_amdgcn_cvt_pk_fp8_f32(c, d, w, true); return w; }
; __device__ __forceinline__ void unpack8(const v4u w, float (&y)[8]) { y[0] = bf_lo(w.x); y[1] = bf_hi(w.x); y[2] = bf_lo(w.y); y[3] = bf_hi(w.y); y[4] = bf_lo(w.z); y[5] = bf_hi(w.z); y[6] = bf_lo(w.w); y[7] = bf_hi(w.w); }
; __device__ __forceinline__ void norm_router_phase(const bf16* x1, const float* g, const float* Wr, unsigned char* XN8, float* AFF, LAS float* WT, int gw, int NGW, int lane, int tid, bool table_ready) {
;     ...
;         for (int i = 0; i < 16; ++i) { const bf16* xr = x1 + (size_t)(row0 + i) * DM + 8 * lane; xa[i] = *(const v4u*)xr; xb[i] = *(const v4u*)(xr + 512); }
; #pragma unroll
;         for (int i = 0; i < 16; ++i) {
;             const float rs = __uint_as_float((unsigned)__builtin_amdgcn_readlane((int)rbits, i));
;             float v[16]; { float t[8]; unpack8(xa[i], t);
; #pragma unroll
;                 for (int j = 0; j < 8; ++j) v[j] = t[j] * (rs * gg[j]);
;                 unpack8(xb[i], t);
; #pragma unroll
;                 for (int j = 0; j < 8; ++j) v[8 + j] = t[j] * (rs * gg[8 + j]); }
;             unsigned char* o = XN8 + (size_t)(row0 + i) * DM + 8 * lane;
;             *(v2u*)o = (v2u){pg8::pk4_fp8(v[0], v[1], v[2], v[3]), pg8::pk4_fp8(v[4], v[5], v[6], v[7])};
;             *(v2u*)(o + 512) = (v2u){pg8::pk4_fp8(v[8], v[9], v[10], v[11]), pg8::pk4_fp8(v[12], v[13], v[14], v[15])};
;         }
	v_lshlrev_b32_e32 v130, 16, v126
	v_mul_f32_e32 v134, s10, v2
	v_and_b32_e32 v126, 0xffff0000, v126
	v_mul_f32_e32 v130, v134, v130
	v_mul_f32_e32 v134, s10, v3
	v_lshlrev_b32_e32 v131, 16, v127
	v_mul_f32_e32 v126, v134, v126
	v_mul_f32_e32 v134, s10, v4
	v_and_b32_e32 v127, 0xffff0000, v127
	v_mul_f32_e32 v131, v134, v131
	v_mul_f32_e32 v134, s10, v5
	v_lshlrev_b32_e32 v132, 16, v128
	v_mul_f32_e32 v127, v134, v127
	v_mul_f32_e32 v134, s10, v6
	v_and_b32_e32 v128, 0xffff0000, v128
	v_mul_f32_e32 v132, v134, v132
	v_mul_f32_e32 v134, s10, v7
	v_lshlrev_b32_e32 v133, 16, v129
	v_mul_f32_e32 v128, v134, v128
	v_mul_f32_e32 v134, s10, v8
	v_and_b32_e32 v129, 0xffff0000, v129
	v_mul_f32_e32 v133, v134, v133
	v_mul_f32_e32 v134, s10, v9
	v_mul_f32_e32 v129, v134, v129
	s_waitcnt vmcnt(30)
	v_lshlrev_b32_e32 v134, 16, v122
	v_mul_f32_e32 v138, s10, v10
	v_and_b32_e32 v122, 0xffff0000, v122
	v_mul_f32_e32 v134, v138, v134
	v_mul_f32_e32 v138, s10, v11
	v_lshlrev_b32_e32 v135, 16, v123
	v_mul_f32_e32 v138, v138, v122
	v_mul_f32_e32 v122, s10, v12
	v_and_b32_e32 v123, 0xffff0000, v123
	v_mul_f32_e32 v135, v122, v135
	v_mul_f32_e32 v122, s10, v13
	v_lshlrev_b32_e32 v136, 16, v124
	v_mul_f32_e32 v139, v122, v123
	v_mul_f32_e32 v122, s10, v14
	v_and_b32_e32 v124, 0xffff0000, v124
	v_mul_f32_e32 v136, v122, v136
	v_mul_f32_e32 v122, s10, v15
	v_lshlrev_b32_e32 v137, 16, v125
	v_mul_f32_e32 v140, v122, v124
	v_mul_f32_e32 v122, s10, v16
	v_and_b32_e32 v125, 0xffff0000, v125
	v_mul_f32_e32 v137, v122, v137
	v_mul_f32_e32 v122, s10, v17
	v_mul_f32_e32 v141, v122, v125
	v_mov_b32_e32 v122, v163
	v_mov_b32_e32 v123, v163
	v_cvt_pk_fp8_f32 v122, v130, v126
	v_cvt_pk_fp8_f32 v123, v132, v128
	v_mov_b32_e32 v124, v163
	v_mov_b32_e32 v125, v163
	v_cvt_pk_fp8_f32 v124, v134, v138
	v_cvt_pk_fp8_f32 v125, v136, v140
	v_cvt_pk_fp8_f32 v122, v131, v127 op_sel:[0,0,1]
	v_cvt_pk_fp8_f32 v123, v133, v129 op_sel:[0,0,1]
	v_cvt_pk_fp8_f32 v124, v135, v139 op_sel:[0,0,1]
	v_cvt_pk_fp8_f32 v125, v137, v141 op_sel:[0,0,1]
	s_lshl_b64 s[10:11], s[22:23], 10
	v_lshl_add_u64 v[126:127], v[170:171], 0, s[10:11]
	v_readlane_b32 s10, v181, 7
	global_store_dwordx2 v[126:127], v[122:123], off
	global_store_dwordx2 v[126:127], v[124:125], off offset:512
	s_waitcnt vmcnt(31)
	v_lshlrev_b32_e32 v122, 16, v118
	v_mul_f32_e32 v126, s10, v2
	v_and_b32_e32 v118, 0xffff0000, v118
	v_mul_f32_e32 v122, v126, v122
	v_mul_f32_e32 v126, s10, v3
	v_lshlrev_b32_e32 v123, 16, v119
	v_mul_f32_e32 v118, v126, v118
	v_mul_f32_e32 v126, s10, v4
	v_and_b32_e32 v119, 0xffff0000, v119
	v_mul_f32_e32 v123, v126, v123
	v_mul_f32_e32 v126, s10, v5
	v_lshlrev_b32_e32 v124, 16, v120
	v_mul_f32_e32 v119, v126, v119
	v_mul_f32_e32 v126, s10, v6
	v_and_b32_e32 v120, 0xffff0000, v120
	v_mul_f32_e32 v124, v126, v124
	v_mul_f32_e32 v126, s10, v7
	v_lshlrev_b32_e32 v125, 16, v121
	v_mul_f32_e32 v120, v126, v120
	v_mul_f32_e32 v126, s10, v8
	v_and_b32_e32 v121, 0xffff0000, v121
	v_mul_f32_e32 v125, v126, v125
	v_mul_f32_e32 v126, s10, v9
	v_mul_f32_e32 v121, v126, v121
	s_waitcnt vmcnt(30)
	v_lshlrev_b32_e32 v126, 16, v114
	v_mul_f32_e32 v130, s10, v10
	v_and_b32_e32 v114, 0xffff0000, v114
	v_mul_f32_e32 v126, v130, v126
	v_mul_f32_e32 v130, s10, v11
	v_lshlrev_b32_e32 v127, 16, v115
	v_mul_f32_e32 v130, v130, v114
	v_mul_f32_e32 v114, s10, v12
	v_and_b32_e32 v115, 0xffff0000, v115
	v_mul_f32_e32 v127, v114, v127
	v_mul_f32_e32 v114, s10, v13
	v_lshlrev_b32_e32 v128, 16, v116
	v_mul_f32_e32 v131, v114, v115
	v_mul_f32_e32 v114, s10, v14
	v_and_b32_e32 v116, 0xffff0000, v116
	v_mul_f32_e32 v128, v114, v128
	v_mul_f32_e32 v114, s10, v15
	v_lshlrev_b32_e32 v129, 16, v117
	v_mul_f32_e32 v132, v114, v116
	v_mul_f32_e32 v114, s10, v16
	v_and_b32_e32 v117, 0xffff0000, v117
	v_mul_f32_e32 v129, v114, v129
	v_mul_f32_e32 v114, s10, v17
	v_mul_f32_e32 v133, v114, v117
	v_mov_b32_e32 v114, v163
	v_mov_b32_e32 v115, v163
	v_cvt_pk_fp8_f32 v114, v122, v118
	v_cvt_pk_fp8_f32 v115, v124, v120
	v_mov_b32_e32 v116, v163
	v_mov_b32_e32 v117, v163
	v_cvt_pk_fp8_f32 v116, v126, v130
	v_cvt_pk_fp8_f32 v117, v128, v132
	v_cvt_pk_fp8_f32 v114, v123, v119 op_sel:[0,0,1]
	v_cvt_pk_fp8_f32 v115, v125, v121 op_sel:[0,0,1]
	v_cvt_pk_fp8_f32 v116, v127, v131 op_sel:[0,0,1]
	v_cvt_pk_fp8_f32 v117, v129, v133 op_sel:[0,0,1]
	s_lshl_b64 s[10:11], s[20:21], 10
	v_lshl_add_u64 v[118:119], v[170:171], 0, s[10:11]
	v_readlane_b32 s10, v181, 8
	global_store_dwordx2 v[118:119], v[114:115], off
	global_store_dwordx2 v[118:119], v[116:117], off offset:512
	s_waitcnt vmcnt(31)
	v_lshlrev_b32_e32 v114, 16, v110
	v_mul_f32_e32 v118, s10, v2
	v_and_b32_e32 v110, 0xffff0000, v110
	v_mul_f32_e32 v114, v118, v114
	v_mul_f32_e32 v118, s10, v3
	v_lshlrev_b32_e32 v115, 16, v111
	v_mul_f32_e32 v110, v118, v110
	v_mul_f32_e32 v118, s10, v4
	v_and_b32_e32 v111, 0xffff0000, v111
	v_mul_f32_e32 v115, v118, v115
	v_mul_f32_e32 v118, s10, v5
	v_lshlrev_b32_e32 v116, 16, v112
	v_mul_f32_e32 v111, v118, v111
	v_mul_f32_e32 v118, s10, v6
	v_and_b32_e32 v112, 0xffff0000, v112
	v_mul_f32_e32 v116, v118, v116
	v_mul_f32_e32 v118, s10, v7
	v_lshlrev_b32_e32 v117, 16, v113
	v_mul_f32_e32 v112, v118, v112
	v_mul_f32_e32 v118, s10, v8
	v_and_b32_e32 v113, 0xffff0000, v113
	v_mul_f32_e32 v117, v118, v117
	v_mul_f32_e32 v118, s10, v9
	v_mul_f32_e32 v113, v118, v113
	s_waitcnt vmcnt(30)
; __device__ __forceinline__ unsigned pk4_fp8(float a, float b, float c, float d) { unsigned w = 0u; w = __builtin_amdgcn_cvt_pk_fp8_f32(a, b, w, false); w = __builtin_amdgcn_cvt_pk_fp8_f32(c, d, w, true); return w; }
; __device__ __forceinline__ void unpack8(const v4u w, float (&y)[8]) { y[0] = bf_lo(w.x); y[1] = bf_hi(w.x); y[2] = bf_lo(w.y); y[3] = bf_hi(w.y); y[4] = bf_lo(w.z); y[5] = bf_hi(w.z); y[6] = bf_lo(w.w); y[7] = bf_hi(w.w); }
; __device__ __forceinline__ void norm_router_phase(const bf16* x1, const float* g, const float* Wr, unsigned char* XN8, float* AFF, LAS float* WT, int gw, int NGW, int lane, int tid, bool table_ready) {
;     ...
;         for (int i = 0; i < 16; ++i) { const bf16* xr = x1 + (size_t)(row0 + i) * DM + 8 * lane; xa[i] = *(const v4u*)xr; xb[i] = *(const v4u*)(xr + 512); }
; #pragma unroll
;         for (int i = 0; i < 16; ++i) {
;             const float rs = __uint_as_float((unsigned)__builtin_amdgcn_readlane((int)rbits, i));
;             float v[16]; { float t[8]; unpack8(xa[i], t);
; #pragma unroll
;                 for (int j = 0; j < 8; ++j) v[j] = t[j] * (rs * gg[j]);
;                 unpack8(xb[i], t);
; #pragma unroll
;                 for (int j = 0; j < 8; ++j) v[8 + j] = t[j] * (rs * gg[8 + j]); }
;             unsigned char* o = XN8 + (size_t)(row0 + i) * DM + 8 * lane;
;             *(v2u*)o = (v2u){pg8::pk4_fp8(v[0], v[1], v[2], v[3]), pg8::pk4_fp8(v[4], v[5], v[6], v[7])};
;             *(v2u*)(o + 512) = (v2u){pg8::pk4_fp8(v[8], v[9], v[10], v[11]), pg8::pk4_fp8(v[12], v[13], v[14], v[15])};
;         }
	v_lshlrev_b32_e32 v118, 16, v106
	v_mul_f32_e32 v122, s10, v10
	v_and_b32_e32 v106, 0xffff0000, v106
	v_mul_f32_e32 v118, v122, v118
	v_mul_f32_e32 v122, s10, v11
	v_lshlrev_b32_e32 v119, 16, v107
	v_mul_f32_e32 v122, v122, v106
	v_mul_f32_e32 v106, s10, v12
	v_and_b32_e32 v107, 0xffff0000, v107
	v_mul_f32_e32 v119, v106, v119
	v_mul_f32_e32 v106, s10, v13
	v_lshlrev_b32_e32 v120, 16, v108
	v_mul_f32_e32 v123, v106, v107
	v_mul_f32_e32 v106, s10, v14
	v_and_b32_e32 v108, 0xffff0000, v108
	v_mul_f32_e32 v120, v106, v120
	v_mul_f32_e32 v106, s10, v15
	v_lshlrev_b32_e32 v121, 16, v109
	v_mul_f32_e32 v124, v106, v108
	v_mul_f32_e32 v106, s10, v16
	v_and_b32_e32 v109, 0xffff0000, v109
	v_mul_f32_e32 v121, v106, v121
	v_mul_f32_e32 v106, s10, v17
	v_mul_f32_e32 v125, v106, v109
	v_mov_b32_e32 v106, v163
	v_mov_b32_e32 v107, v163
	v_cvt_pk_fp8_f32 v106, v114, v110
	v_cvt_pk_fp8_f32 v107, v116, v112
	v_mov_b32_e32 v108, v163
	v_mov_b32_e32 v109, v163
	v_cvt_pk_fp8_f32 v108, v118, v122
	v_cvt_pk_fp8_f32 v109, v120, v124
	v_cvt_pk_fp8_f32 v106, v115, v111 op_sel:[0,0,1]
	v_cvt_pk_fp8_f32 v107, v117, v113 op_sel:[0,0,1]
	v_cvt_pk_fp8_f32 v108, v119, v123 op_sel:[0,0,1]
	v_cvt_pk_fp8_f32 v109, v121, v125 op_sel:[0,0,1]
	s_lshl_b64 s[10:11], s[18:19], 10
	v_lshl_add_u64 v[110:111], v[170:171], 0, s[10:11]
	v_readlane_b32 s10, v181, 9
	global_store_dwordx2 v[110:111], v[106:107], off
	global_store_dwordx2 v[110:111], v[108:109], off offset:512
	s_waitcnt vmcnt(31)
	v_lshlrev_b32_e32 v106, 16, v102
	v_mul_f32_e32 v110, s10, v2
	v_and_b32_e32 v102, 0xffff0000, v102
	v_mul_f32_e32 v106, v110, v106
	v_mul_f32_e32 v110, s10, v3
	v_lshlrev_b32_e32 v107, 16, v103
	v_mul_f32_e32 v102, v110, v102
	v_mul_f32_e32 v110, s10, v4
	v_and_b32_e32 v103, 0xffff0000, v103
	v_mul_f32_e32 v107, v110, v107
	v_mul_f32_e32 v110, s10, v5
	v_lshlrev_b32_e32 v108, 16, v104
	v_mul_f32_e32 v103, v110, v103
	v_mul_f32_e32 v110, s10, v6
	v_and_b32_e32 v104, 0xffff0000, v104
	v_mul_f32_e32 v108, v110, v108
	v_mul_f32_e32 v110, s10, v7
	v_lshlrev_b32_e32 v109, 16, v105
	v_mul_f32_e32 v104, v110, v104
	v_mul_f32_e32 v110, s10, v8
	v_and_b32_e32 v105, 0xffff0000, v105
	v_mul_f32_e32 v109, v110, v109
	v_mul_f32_e32 v110, s10, v9
	v_mul_f32_e32 v105, v110, v105
	s_waitcnt vmcnt(30)
	v_lshlrev_b32_e32 v110, 16, v98
	v_mul_f32_e32 v114, s10, v10
	v_and_b32_e32 v98, 0xffff0000, v98
	v_mul_f32_e32 v110, v114, v110
	v_mul_f32_e32 v114, s10, v11
	v_lshlrev_b32_e32 v111, 16, v99
	v_mul_f32_e32 v114, v114, v98
	v_mul_f32_e32 v98, s10, v12
	v_and_b32_e32 v99, 0xffff0000, v99
	v_mul_f32_e32 v111, v98, v111
	v_mul_f32_e32 v98, s10, v13
	v_lshlrev_b32_e32 v112, 16, v100
	v_mul_f32_e32 v115, v98, v99
	v_mul_f32_e32 v98, s10, v14
	v_and_b32_e32 v100, 0xffff0000, v100
	v_mul_f32_e32 v112, v98, v112
	v_mul_f32_e32 v98, s10, v15
	v_lshlrev_b32_e32 v113, 16, v101
	v_mul_f32_e32 v116, v98, v100
	v_mul_f32_e32 v98, s10, v16
	v_and_b32_e32 v101, 0xffff0000, v101
	v_mul_f32_e32 v113, v98, v113
	v_mul_f32_e32 v98, s10, v17
	v_mul_f32_e32 v117, v98, v101
	v_mov_b32_e32 v98, v163
	v_mov_b32_e32 v99, v163
	v_cvt_pk_fp8_f32 v98, v106, v102
	v_cvt_pk_fp8_f32 v99, v108, v104
	v_mov_b32_e32 v100, v163
	v_mov_b32_e32 v101, v163
	v_cvt_pk_fp8_f32 v100, v110, v114
	v_cvt_pk_fp8_f32 v101, v112, v116
	v_cvt_pk_fp8_f32 v98, v107, v103 op_sel:[0,0,1]
	v_cvt_pk_fp8_f32 v99, v109, v105 op_sel:[0,0,1]
	v_cvt_pk_fp8_f32 v100, v111, v115 op_sel:[0,0,1]
	v_cvt_pk_fp8_f32 v101, v113, v117 op_sel:[0,0,1]
	s_lshl_b64 s[10:11], s[16:17], 10
	v_lshl_add_u64 v[102:103], v[170:171], 0, s[10:11]
	v_readlane_b32 s10, v181, 10
	global_store_dwordx2 v[102:103], v[98:99], off
	global_store_dwordx2 v[102:103], v[100:101], off offset:512
	s_waitcnt vmcnt(31)
	v_lshlrev_b32_e32 v98, 16, v94
	v_mul_f32_e32 v102, s10, v2
	v_and_b32_e32 v94, 0xffff0000, v94
	v_mul_f32_e32 v98, v102, v98
	v_mul_f32_e32 v102, s10, v3
	v_lshlrev_b32_e32 v99, 16, v95
	v_mul_f32_e32 v94, v102, v94
	v_mul_f32_e32 v102, s10, v4
	v_and_b32_e32 v95, 0xffff0000, v95
	v_mul_f32_e32 v99, v102, v99
	v_mul_f32_e32 v102, s10, v5
	v_lshlrev_b32_e32 v100, 16, v96
	v_mul_f32_e32 v95, v102, v95
	v_mul_f32_e32 v102, s10, v6
	v_and_b32_e32 v96, 0xffff0000, v96
	v_mul_f32_e32 v100, v102, v100
	v_mul_f32_e32 v102, s10, v7
	v_lshlrev_b32_e32 v101, 16, v97
	v_mul_f32_e32 v96, v102, v96
	v_mul_f32_e32 v102, s10, v8
	v_and_b32_e32 v97, 0xffff0000, v97
	v_mul_f32_e32 v101, v102, v101
	v_mul_f32_e32 v102, s10, v9
	v_mul_f32_e32 v97, v102, v97
	s_waitcnt vmcnt(30)
	v_lshlrev_b32_e32 v102, 16, v90
	v_mul_f32_e32 v106, s10, v10
	v_and_b32_e32 v90, 0xffff0000, v90
	v_mul_f32_e32 v102, v106, v102
	v_mul_f32_e32 v106, s10, v11
	v_lshlrev_b32_e32 v103, 16, v91
	v_mul_f32_e32 v106, v106, v90
	v_mul_f32_e32 v90, s10, v12
	v_and_b32_e32 v91, 0xffff0000, v91
	v_mul_f32_e32 v103, v90, v103
	v_mul_f32_e32 v90, s10, v13
	v_lshlrev_b32_e32 v104, 16, v92
	v_mul_f32_e32 v107, v90, v91
	v_mul_f32_e32 v90, s10, v14
	v_and_b32_e32 v92, 0xffff0000, v92
	v_mul_f32_e32 v104, v90, v104
	v_mul_f32_e32 v90, s10, v15
	v_lshlrev_b32_e32 v105, 16, v93
	v_mul_f32_e32 v108, v90, v92
	v_mul_f32_e32 v90, s10, v16
	v_and_b32_e32 v93, 0xffff0000, v93
	v_mul_f32_e32 v105, v90, v105
	v_mul_f32_e32 v90, s10, v17
	v_mul_f32_e32 v109, v90, v93
	v_mov_b32_e32 v90, v163
	v_mov_b32_e32 v91, v163
	v_cvt_pk_fp8_f32 v90, v98, v94
	v_cvt_pk_fp8_f32 v91, v100, v96
	v_mov_b32_e32 v92, v163
	v_mov_b32_e32 v93, v163
	v_cvt_pk_fp8_f32 v92, v102, v106
	v_cvt_pk_fp8_f32 v93, v104, v108
	v_cvt_pk_fp8_f32 v90, v99, v95 op_sel:[0,0,1]
	v_cvt_pk_fp8_f32 v91, v101, v97 op_sel:[0,0,1]
	v_cvt_pk_fp8_f32 v92, v103, v107 op_sel:[0,0,1]
	v_cvt_pk_fp8_f32 v93, v105, v109 op_sel:[0,0,1]
	s_lshl_b64 s[10:11], s[14:15], 10
	v_lshl_add_u64 v[94:95], v[170:171], 0, s[10:11]
	v_readlane_b32 s10, v181, 11
	global_store_dwordx2 v[94:95], v[90:91], off
	global_store_dwordx2 v[94:95], v[92:93], off offset:512
	s_waitcnt vmcnt(31)
; __device__ __forceinline__ unsigned pk4_fp8(float a, float b, float c, float d) { unsigned w = 0u; w = __builtin_amdgcn_cvt_pk_fp8_f32(a, b, w, false); w = __builtin_amdgcn_cvt_pk_fp8_f32(c, d, w, true); return w; }
; __device__ __forceinline__ void unpack8(const v4u w, float (&y)[8]) { y[0] = bf_lo(w.x); y[1] = bf_hi(w.x); y[2] = bf_lo(w.y); y[3] = bf_hi(w.y); y[4] = bf_lo(w.z); y[5] = bf_hi(w.z); y[6] = bf_lo(w.w); y[7] = bf_hi(w.w); }
; __device__ __forceinline__ void norm_router_phase(const bf16* x1, const float* g, const float* Wr, unsigned char* XN8, float* AFF, LAS float* WT, int gw, int NGW, int lane, int tid, bool table_ready) {
;     ...
;         for (int i = 0; i < 16; ++i) { const bf16* xr = x1 + (size_t)(row0 + i) * DM + 8 * lane; xa[i] = *(const v4u*)xr; xb[i] = *(const v4u*)(xr + 512); }
; #pragma unroll
;         for (int i = 0; i < 16; ++i) {
;             const float rs = __uint_as_float((unsigned)__builtin_amdgcn_readlane((int)rbits, i));
;             float v[16]; { float t[8]; unpack8(xa[i], t);
; #pragma unroll
;                 for (int j = 0; j < 8; ++j) v[j] = t[j] * (rs * gg[j]);
;                 unpack8(xb[i], t);
; #pragma unroll
;                 for (int j = 0; j < 8; ++j) v[8 + j] = t[j] * (rs * gg[8 + j]); }
;             unsigned char* o = XN8 + (size_t)(row0 + i) * DM + 8 * lane;
;             *(v2u*)o = (v2u){pg8::pk4_fp8(v[0], v[1], v[2], v[3]), pg8::pk4_fp8(v[4], v[5], v[6], v[7])};
;             *(v2u*)(o + 512) = (v2u){pg8::pk4_fp8(v[8], v[9], v[10], v[11]), pg8::pk4_fp8(v[12], v[13], v[14], v[15])};
;         }
	v_lshlrev_b32_e32 v90, 16, v86
	v_mul_f32_e32 v94, s10, v2
	v_and_b32_e32 v86, 0xffff0000, v86
	v_mul_f32_e32 v90, v94, v90
	v_mul_f32_e32 v94, s10, v3
	v_lshlrev_b32_e32 v91, 16, v87
	v_mul_f32_e32 v86, v94, v86
	v_mul_f32_e32 v94, s10, v4
	v_and_b32_e32 v87, 0xffff0000, v87
	v_mul_f32_e32 v91, v94, v91
	v_mul_f32_e32 v94, s10, v5
	v_lshlrev_b32_e32 v92, 16, v88
	v_mul_f32_e32 v87, v94, v87
	v_mul_f32_e32 v94, s10, v6
	v_and_b32_e32 v88, 0xffff0000, v88
	v_mul_f32_e32 v92, v94, v92
	v_mul_f32_e32 v94, s10, v7
	v_lshlrev_b32_e32 v93, 16, v89
	v_mul_f32_e32 v88, v94, v88
	v_mul_f32_e32 v94, s10, v8
	v_and_b32_e32 v89, 0xffff0000, v89
	v_mul_f32_e32 v93, v94, v93
	v_mul_f32_e32 v94, s10, v9
	v_mul_f32_e32 v89, v94, v89
	s_waitcnt vmcnt(30)
	v_lshlrev_b32_e32 v94, 16, v82
	v_mul_f32_e32 v98, s10, v10
	v_and_b32_e32 v82, 0xffff0000, v82
	v_mul_f32_e32 v94, v98, v94
	v_mul_f32_e32 v98, s10, v11
	v_lshlrev_b32_e32 v95, 16, v83
	v_mul_f32_e32 v98, v98, v82
	v_mul_f32_e32 v82, s10, v12
	v_and_b32_e32 v83, 0xffff0000, v83
	v_mul_f32_e32 v95, v82, v95
	v_mul_f32_e32 v82, s10, v13
	v_lshlrev_b32_e32 v96, 16, v84
	v_mul_f32_e32 v99, v82, v83
	v_mul_f32_e32 v82, s10, v14
	v_and_b32_e32 v84, 0xffff0000, v84
	v_mul_f32_e32 v96, v82, v96
	v_mul_f32_e32 v82, s10, v15
	v_lshlrev_b32_e32 v97, 16, v85
	v_mul_f32_e32 v100, v82, v84
	v_mul_f32_e32 v82, s10, v16
	v_and_b32_e32 v85, 0xffff0000, v85
	v_mul_f32_e32 v97, v82, v97
	v_mul_f32_e32 v82, s10, v17
	v_mul_f32_e32 v101, v82, v85
	v_mov_b32_e32 v82, v163
	v_mov_b32_e32 v83, v163
	v_cvt_pk_fp8_f32 v82, v90, v86
	v_cvt_pk_fp8_f32 v83, v92, v88
	v_mov_b32_e32 v84, v163
	v_mov_b32_e32 v85, v163
	v_cvt_pk_fp8_f32 v84, v94, v98
	v_cvt_pk_fp8_f32 v85, v96, v100
	v_cvt_pk_fp8_f32 v82, v91, v87 op_sel:[0,0,1]
	v_cvt_pk_fp8_f32 v83, v93, v89 op_sel:[0,0,1]
	v_cvt_pk_fp8_f32 v84, v95, v99 op_sel:[0,0,1]
	v_cvt_pk_fp8_f32 v85, v97, v101 op_sel:[0,0,1]
	s_lshl_b64 s[10:11], s[12:13], 10
	v_lshl_add_u64 v[86:87], v[170:171], 0, s[10:11]
	v_readlane_b32 s10, v181, 12
	global_store_dwordx2 v[86:87], v[82:83], off
	global_store_dwordx2 v[86:87], v[84:85], off offset:512
	s_waitcnt vmcnt(31)
	v_lshlrev_b32_e32 v82, 16, v78
	v_mul_f32_e32 v86, s10, v2
	v_and_b32_e32 v78, 0xffff0000, v78
	v_mul_f32_e32 v82, v86, v82
	v_mul_f32_e32 v86, s10, v3
	v_lshlrev_b32_e32 v83, 16, v79
	v_mul_f32_e32 v78, v86, v78
	v_mul_f32_e32 v86, s10, v4
	v_and_b32_e32 v79, 0xffff0000, v79
	v_mul_f32_e32 v83, v86, v83
	v_mul_f32_e32 v86, s10, v5
	v_lshlrev_b32_e32 v84, 16, v80
	v_mul_f32_e32 v79, v86, v79
	v_mul_f32_e32 v86, s10, v6
	v_and_b32_e32 v80, 0xffff0000, v80
	v_mul_f32_e32 v84, v86, v84
	v_mul_f32_e32 v86, s10, v7
	v_lshlrev_b32_e32 v85, 16, v81
	v_mul_f32_e32 v80, v86, v80
	v_mul_f32_e32 v86, s10, v8
	v_and_b32_e32 v81, 0xffff0000, v81
	v_mul_f32_e32 v85, v86, v85
	v_mul_f32_e32 v86, s10, v9
	v_mul_f32_e32 v81, v86, v81
	s_waitcnt vmcnt(30)
	v_lshlrev_b32_e32 v86, 16, v74
	v_mul_f32_e32 v90, s10, v10
	v_and_b32_e32 v74, 0xffff0000, v74
	v_mul_f32_e32 v86, v90, v86
	v_mul_f32_e32 v90, s10, v11
	v_lshlrev_b32_e32 v87, 16, v75
	v_mul_f32_e32 v90, v90, v74
	v_mul_f32_e32 v74, s10, v12
	v_and_b32_e32 v75, 0xffff0000, v75
	v_mul_f32_e32 v87, v74, v87
	v_mul_f32_e32 v74, s10, v13
	v_lshlrev_b32_e32 v88, 16, v76
	v_mul_f32_e32 v91, v74, v75
	v_mul_f32_e32 v74, s10, v14
	v_and_b32_e32 v76, 0xffff0000, v76
	v_mul_f32_e32 v88, v74, v88
	v_mul_f32_e32 v74, s10, v15
	v_lshlrev_b32_e32 v89, 16, v77
	v_mul_f32_e32 v92, v74, v76
	v_mul_f32_e32 v74, s10, v16
	v_and_b32_e32 v77, 0xffff0000, v77
	v_mul_f32_e32 v89, v74, v89
	v_mul_f32_e32 v74, s10, v17
	v_mul_f32_e32 v93, v74, v77
	v_mov_b32_e32 v74, v163
	v_mov_b32_e32 v75, v163
	v_cvt_pk_fp8_f32 v74, v82, v78
	v_cvt_pk_fp8_f32 v75, v84, v80
	v_mov_b32_e32 v76, v163
	v_mov_b32_e32 v77, v163
	v_cvt_pk_fp8_f32 v76, v86, v90
	v_cvt_pk_fp8_f32 v77, v88, v92
	v_cvt_pk_fp8_f32 v74, v83, v79 op_sel:[0,0,1]
	v_cvt_pk_fp8_f32 v75, v85, v81 op_sel:[0,0,1]
	v_cvt_pk_fp8_f32 v76, v87, v91 op_sel:[0,0,1]
	v_cvt_pk_fp8_f32 v77, v89, v93 op_sel:[0,0,1]
	v_lshl_add_u64 v[78:79], v[170:171], 0, s[8:9]
	v_readlane_b32 s8, v181, 13
	global_store_dwordx2 v[78:79], v[74:75], off
	global_store_dwordx2 v[78:79], v[76:77], off offset:512
	s_waitcnt vmcnt(31)
	v_lshlrev_b32_e32 v74, 16, v70
	v_mul_f32_e32 v78, s8, v2
	v_and_b32_e32 v70, 0xffff0000, v70
	v_mul_f32_e32 v74, v78, v74
	v_mul_f32_e32 v78, s8, v3
	v_lshlrev_b32_e32 v75, 16, v71
	v_mul_f32_e32 v70, v78, v70
	v_mul_f32_e32 v78, s8, v4
	v_and_b32_e32 v71, 0xffff0000, v71
	v_mul_f32_e32 v75, v78, v75
	v_mul_f32_e32 v78, s8, v5
	v_lshlrev_b32_e32 v76, 16, v72
	v_mul_f32_e32 v71, v78, v71
	v_mul_f32_e32 v78, s8, v6
	v_and_b32_e32 v72, 0xffff0000, v72
	v_mul_f32_e32 v76, v78, v76
	v_mul_f32_e32 v78, s8, v7
	v_lshlrev_b32_e32 v77, 16, v73
	v_mul_f32_e32 v72, v78, v72
	v_mul_f32_e32 v78, s8, v8
	v_and_b32_e32 v73, 0xffff0000, v73
	v_mul_f32_e32 v77, v78, v77
	v_mul_f32_e32 v78, s8, v9
	v_mul_f32_e32 v73, v78, v73
	s_waitcnt vmcnt(30)
; __device__ __forceinline__ unsigned pk4_fp8(float a, float b, float c, float d) { unsigned w = 0u; w = __builtin_amdgcn_cvt_pk_fp8_f32(a, b, w, false); w = __builtin_amdgcn_cvt_pk_fp8_f32(c, d, w, true); return w; }
; __device__ __forceinline__ void unpack8(const v4u w, float (&y)[8]) { y[0] = bf_lo(w.x); y[1] = bf_hi(w.x); y[2] = bf_lo(w.y); y[3] = bf_hi(w.y); y[4] = bf_lo(w.z); y[5] = bf_hi(w.z); y[6] = bf_lo(w.w); y[7] = bf_hi(w.w); }
; __device__ __forceinline__ void norm_router_phase(const bf16* x1, const float* g, const float* Wr, unsigned char* XN8, float* AFF, LAS float* WT, int gw, int NGW, int lane, int tid, bool table_ready) {
;     ...
;     for (int grp = gw; grp < NTOK / 16; grp += NGW) {
;     ...
;         for (int i = 0; i < 16; ++i) { const bf16* xr = x1 + (size_t)(row0 + i) * DM + 8 * lane; xa[i] = *(const v4u*)xr; xb[i] = *(const v4u*)(xr + 512); }
; #pragma unroll
;         for (int i = 0; i < 16; ++i) {
;             const float rs = __uint_as_float((unsigned)__builtin_amdgcn_readlane((int)rbits, i));
;             float v[16]; { float t[8]; unpack8(xa[i], t);
; #pragma unroll
;                 for (int j = 0; j < 8; ++j) v[j] = t[j] * (rs * gg[j]);
;                 unpack8(xb[i], t);
; #pragma unroll
;                 for (int j = 0; j < 8; ++j) v[8 + j] = t[j] * (rs * gg[8 + j]); }
;             unsigned char* o = XN8 + (size_t)(row0 + i) * DM + 8 * lane;
;             *(v2u*)o = (v2u){pg8::pk4_fp8(v[0], v[1], v[2], v[3]), pg8::pk4_fp8(v[4], v[5], v[6], v[7])};
;             *(v2u*)(o + 512) = (v2u){pg8::pk4_fp8(v[8], v[9], v[10], v[11]), pg8::pk4_fp8(v[12], v[13], v[14], v[15])};
;         }
	v_lshlrev_b32_e32 v78, 16, v66
	v_mul_f32_e32 v82, s8, v10
	v_and_b32_e32 v66, 0xffff0000, v66
	v_mul_f32_e32 v78, v82, v78
	v_mul_f32_e32 v82, s8, v11
	v_lshlrev_b32_e32 v79, 16, v67
	v_mul_f32_e32 v82, v82, v66
	v_mul_f32_e32 v66, s8, v12
	v_and_b32_e32 v67, 0xffff0000, v67
	v_mul_f32_e32 v79, v66, v79
	v_mul_f32_e32 v66, s8, v13
	v_lshlrev_b32_e32 v80, 16, v68
	v_mul_f32_e32 v83, v66, v67
	v_mul_f32_e32 v66, s8, v14
	v_and_b32_e32 v68, 0xffff0000, v68
	v_mul_f32_e32 v80, v66, v80
	v_mul_f32_e32 v66, s8, v15
	v_lshlrev_b32_e32 v81, 16, v69
	v_mul_f32_e32 v84, v66, v68
	v_mul_f32_e32 v66, s8, v16
	v_and_b32_e32 v69, 0xffff0000, v69
	v_mul_f32_e32 v81, v66, v81
	v_mul_f32_e32 v66, s8, v17
	v_mul_f32_e32 v85, v66, v69
	v_mov_b32_e32 v66, v163
	v_mov_b32_e32 v67, v163
	v_cvt_pk_fp8_f32 v66, v74, v70
	v_cvt_pk_fp8_f32 v67, v76, v72
	v_mov_b32_e32 v68, v163
	v_mov_b32_e32 v69, v163
	v_cvt_pk_fp8_f32 v68, v78, v82
	v_cvt_pk_fp8_f32 v69, v80, v84
	v_cvt_pk_fp8_f32 v66, v75, v71 op_sel:[0,0,1]
	v_cvt_pk_fp8_f32 v67, v77, v73 op_sel:[0,0,1]
	v_cvt_pk_fp8_f32 v68, v79, v83 op_sel:[0,0,1]
	v_cvt_pk_fp8_f32 v69, v81, v85 op_sel:[0,0,1]
	v_lshl_add_u64 v[70:71], v[170:171], 0, s[6:7]
	v_readlane_b32 s6, v181, 14
	global_store_dwordx2 v[70:71], v[66:67], off
	global_store_dwordx2 v[70:71], v[68:69], off offset:512
	s_waitcnt vmcnt(31)
	v_lshlrev_b32_e32 v66, 16, v62
	v_mul_f32_e32 v70, s6, v2
	v_and_b32_e32 v62, 0xffff0000, v62
	v_mul_f32_e32 v66, v70, v66
	v_mul_f32_e32 v70, s6, v3
	v_lshlrev_b32_e32 v67, 16, v63
	v_mul_f32_e32 v62, v70, v62
	v_mul_f32_e32 v70, s6, v4
	v_and_b32_e32 v63, 0xffff0000, v63
	v_mul_f32_e32 v67, v70, v67
	v_mul_f32_e32 v70, s6, v5
	v_lshlrev_b32_e32 v68, 16, v64
	v_mul_f32_e32 v63, v70, v63
	v_mul_f32_e32 v70, s6, v6
	v_and_b32_e32 v64, 0xffff0000, v64
	v_mul_f32_e32 v68, v70, v68
	v_mul_f32_e32 v70, s6, v7
	v_lshlrev_b32_e32 v69, 16, v65
	v_mul_f32_e32 v64, v70, v64
	v_mul_f32_e32 v70, s6, v8
	v_and_b32_e32 v65, 0xffff0000, v65
	v_mul_f32_e32 v69, v70, v69
	v_mul_f32_e32 v70, s6, v9
	v_mul_f32_e32 v65, v70, v65
	s_waitcnt vmcnt(30)
	v_lshlrev_b32_e32 v70, 16, v58
	v_mul_f32_e32 v74, s6, v10
	v_and_b32_e32 v58, 0xffff0000, v58
	v_mul_f32_e32 v70, v74, v70
	v_mul_f32_e32 v74, s6, v11
	v_lshlrev_b32_e32 v71, 16, v59
	v_mul_f32_e32 v74, v74, v58
	v_mul_f32_e32 v58, s6, v12
	v_and_b32_e32 v59, 0xffff0000, v59
	v_mul_f32_e32 v71, v58, v71
	v_mul_f32_e32 v58, s6, v13
	v_lshlrev_b32_e32 v72, 16, v60
	v_mul_f32_e32 v75, v58, v59
	v_mul_f32_e32 v58, s6, v14
	v_and_b32_e32 v60, 0xffff0000, v60
	v_mul_f32_e32 v72, v58, v72
	v_mul_f32_e32 v58, s6, v15
	v_lshlrev_b32_e32 v73, 16, v61
	v_mul_f32_e32 v76, v58, v60
	v_mul_f32_e32 v58, s6, v16
	v_and_b32_e32 v61, 0xffff0000, v61
	v_mul_f32_e32 v73, v58, v73
	v_mul_f32_e32 v58, s6, v17
	v_mul_f32_e32 v77, v58, v61
	v_mov_b32_e32 v58, v163
	v_mov_b32_e32 v59, v163
	v_cvt_pk_fp8_f32 v58, v66, v62
	v_cvt_pk_fp8_f32 v59, v68, v64
	v_mov_b32_e32 v60, v163
	v_mov_b32_e32 v61, v163
	v_cvt_pk_fp8_f32 v60, v70, v74
	v_cvt_pk_fp8_f32 v61, v72, v76
	v_cvt_pk_fp8_f32 v58, v67, v63 op_sel:[0,0,1]
	v_cvt_pk_fp8_f32 v59, v69, v65 op_sel:[0,0,1]
	v_cvt_pk_fp8_f32 v60, v71, v75 op_sel:[0,0,1]
	v_cvt_pk_fp8_f32 v61, v73, v77 op_sel:[0,0,1]
	v_lshl_add_u64 v[62:63], v[170:171], 0, s[4:5]
	v_readlane_b32 s4, v181, 15
	global_store_dwordx2 v[62:63], v[58:59], off
	global_store_dwordx2 v[62:63], v[60:61], off offset:512
	s_waitcnt vmcnt(31)
	v_lshlrev_b32_e32 v58, 16, v54
	v_mul_f32_e32 v62, s4, v2
	v_and_b32_e32 v54, 0xffff0000, v54
	v_mul_f32_e32 v58, v62, v58
	v_mul_f32_e32 v62, s4, v3
	v_lshlrev_b32_e32 v59, 16, v55
	v_mul_f32_e32 v54, v62, v54
	v_mul_f32_e32 v62, s4, v4
	v_and_b32_e32 v55, 0xffff0000, v55
	v_mul_f32_e32 v59, v62, v59
	v_mul_f32_e32 v62, s4, v5
	v_lshlrev_b32_e32 v60, 16, v56
	v_mul_f32_e32 v55, v62, v55
	v_mul_f32_e32 v62, s4, v6
	v_and_b32_e32 v56, 0xffff0000, v56
	v_mul_f32_e32 v60, v62, v60
	v_mul_f32_e32 v62, s4, v7
	v_lshlrev_b32_e32 v61, 16, v57
	v_mul_f32_e32 v56, v62, v56
	v_mul_f32_e32 v62, s4, v8
	v_and_b32_e32 v57, 0xffff0000, v57
	v_mul_f32_e32 v61, v62, v61
	v_mul_f32_e32 v62, s4, v9
	v_mul_f32_e32 v57, v62, v57
	s_waitcnt vmcnt(30)
	v_lshlrev_b32_e32 v62, 16, v50
	v_mul_f32_e32 v66, s4, v10
	v_and_b32_e32 v50, 0xffff0000, v50
	v_mul_f32_e32 v62, v66, v62
	v_mul_f32_e32 v66, s4, v11
	v_lshlrev_b32_e32 v63, 16, v51
	v_mul_f32_e32 v66, v66, v50
	v_mul_f32_e32 v50, s4, v12
	v_and_b32_e32 v51, 0xffff0000, v51
	v_mul_f32_e32 v63, v50, v63
	v_mul_f32_e32 v50, s4, v13
	v_lshlrev_b32_e32 v64, 16, v52
	v_mul_f32_e32 v67, v50, v51
	v_mul_f32_e32 v50, s4, v14
	v_and_b32_e32 v52, 0xffff0000, v52
	v_mul_f32_e32 v64, v50, v64
	v_mul_f32_e32 v50, s4, v15
	v_lshlrev_b32_e32 v65, 16, v53
	v_mul_f32_e32 v68, v50, v52
	v_mul_f32_e32 v50, s4, v16
	v_and_b32_e32 v53, 0xffff0000, v53
	v_mul_f32_e32 v65, v50, v65
	v_mul_f32_e32 v50, s4, v17
	v_mul_f32_e32 v69, v50, v53
	v_mov_b32_e32 v50, v163
	v_mov_b32_e32 v51, v163
	v_cvt_pk_fp8_f32 v50, v58, v54
	v_cvt_pk_fp8_f32 v51, v60, v56
	v_mov_b32_e32 v52, v163
	v_mov_b32_e32 v53, v163
	v_cvt_pk_fp8_f32 v52, v62, v66
	v_cvt_pk_fp8_f32 v53, v64, v68
	v_cvt_pk_fp8_f32 v50, v59, v55 op_sel:[0,0,1]
	v_cvt_pk_fp8_f32 v51, v61, v57 op_sel:[0,0,1]
	v_cvt_pk_fp8_f32 v52, v63, v67 op_sel:[0,0,1]
	v_cvt_pk_fp8_f32 v53, v65, v69 op_sel:[0,0,1]
	v_lshl_add_u64 v[54:55], v[170:171], 0, s[2:3]
	v_readlane_b32 s2, v254, 52
	s_add_i32 s37, s37, s2
	s_cmpk_gt_i32 s37, 0x7ff
	global_store_dwordx2 v[54:55], v[50:51], off
	global_store_dwordx2 v[54:55], v[52:53], off offset:512
	s_cbranch_scc1 .LBB0_550

; __device__ __forceinline__ void norm_router_phase(const bf16* x1, const float* g, const float* Wr, unsigned char* XN8, float* AFF, LAS float* WT, int gw, int NGW, int lane, int tid, bool table_ready) {
;     ...
;         ss += __shfl_xor(ss, 16); ss += __shfl_xor(ss, 32);
;         const float rstd = 1.0f / sqrtf(ss * (1.f / DM) + RMS_EPS);
;         float lg[4], mx;
; #pragma unroll
;         for (int r = 0; r < 4; ++r) lg[r] = (acc0[r] + acc1[r]) * rstd;
;         mx = fmaxf(fmaxf(lg[0], lg[1]), fmaxf(lg[2], lg[3])); mx = fmaxf(mx, __shfl_xor(mx, 16)); mx = fmaxf(mx, __shfl_xor(mx, 32));
;         float ex[4], sm = 0.f;
; #pragma unroll
;         for (int r = 0; r < 4; ++r) { ex[r] = __builtin_amdgcn_exp2f((lg[r] - mx) * LOG2E); sm += ex[r]; }
;         sm += __shfl_xor(sm, 16); sm += __shfl_xor(sm, 32);
;         { const int row = row0 + ti; const float inv = 1.0f / sm;
; #pragma unroll
;           for (int r = 0; r < 4; ++r) AFF[((size_t)(4 * kq + r) * NB + (row >> 13)) * SEQ + (row & (SEQ - 1))] = ex[r] * inv; }
;         const unsigned rbits = __float_as_uint(rstd);
;         v4u xa[16], xb[16];
; #pragma unroll
;         for (int i = 0; i < 16; ++i) { const bf16* xr = x1 + (size_t)(row0 + i) * DM + 8 * lane; xa[i] = *(const v4u*)xr; xb[i] = *(const v4u*)(xr + 512); }
.LBB0_1274:
	s_mov_b32 s98, s14
	s_ashr_i32 s99, s98, 31
	s_lshl_b64 s[100:101], s[98:99], 11
	v_lshl_add_u64 v[214:215], v[168:169], 0, s[100:101]
	global_load_dwordx4 v[188:191], v[214:215], off
	global_load_dwordx4 v[192:195], v[214:215], off offset:1024
	s_or_b32 s98, s14, 1
	s_ashr_i32 s99, s98, 31
	s_lshl_b64 s[100:101], s[98:99], 11
	v_lshl_add_u64 v[214:215], v[168:169], 0, s[100:101]
	global_load_dwordx4 v[196:199], v[214:215], off
	global_load_dwordx4 v[200:203], v[214:215], off offset:1024
	s_or_b32 s98, s14, 2
	s_ashr_i32 s99, s98, 31
	s_lshl_b64 s[100:101], s[98:99], 11
	v_lshl_add_u64 v[214:215], v[168:169], 0, s[100:101]
	global_load_dwordx4 v[158:161], v[214:215], off
	global_load_dwordx4 v[154:157], v[214:215], off offset:1024
	s_or_b32 s98, s14, 3
	s_ashr_i32 s99, s98, 31
	s_lshl_b64 s[100:101], s[98:99], 11
	v_lshl_add_u64 v[214:215], v[168:169], 0, s[100:101]
	global_load_dwordx4 v[150:153], v[214:215], off
	global_load_dwordx4 v[146:149], v[214:215], off offset:1024
	s_or_b32 s98, s14, 4
	s_ashr_i32 s99, s98, 31
	s_lshl_b64 s[100:101], s[98:99], 11
	v_lshl_add_u64 v[214:215], v[168:169], 0, s[100:101]
	global_load_dwordx4 v[142:145], v[214:215], off
	global_load_dwordx4 v[138:141], v[214:215], off offset:1024
	s_or_b32 s98, s14, 5
	s_ashr_i32 s99, s98, 31
	s_lshl_b64 s[100:101], s[98:99], 11
	v_lshl_add_u64 v[214:215], v[168:169], 0, s[100:101]
	global_load_dwordx4 v[134:137], v[214:215], off
	global_load_dwordx4 v[130:133], v[214:215], off offset:1024
	s_or_b32 s98, s14, 6
	s_ashr_i32 s99, s98, 31
	s_lshl_b64 s[100:101], s[98:99], 11
	v_lshl_add_u64 v[214:215], v[168:169], 0, s[100:101]
	global_load_dwordx4 v[126:129], v[214:215], off
	global_load_dwordx4 v[122:125], v[214:215], off offset:1024
	s_or_b32 s98, s14, 7
	s_ashr_i32 s99, s98, 31
	s_lshl_b64 s[100:101], s[98:99], 11
	v_lshl_add_u64 v[214:215], v[168:169], 0, s[100:101]
	global_load_dwordx4 v[118:121], v[214:215], off
	global_load_dwordx4 v[114:117], v[214:215], off offset:1024
	s_or_b32 s98, s14, 8
	s_ashr_i32 s99, s98, 31
	s_lshl_b64 s[100:101], s[98:99], 11
	v_lshl_add_u64 v[214:215], v[168:169], 0, s[100:101]
	global_load_dwordx4 v[110:113], v[214:215], off
	global_load_dwordx4 v[106:109], v[214:215], off offset:1024
	s_or_b32 s98, s14, 9
	s_ashr_i32 s99, s98, 31
	s_lshl_b64 s[100:101], s[98:99], 11
	v_lshl_add_u64 v[214:215], v[168:169], 0, s[100:101]
	global_load_dwordx4 v[102:105], v[214:215], off
	global_load_dwordx4 v[98:101], v[214:215], off offset:1024
	ds_bpermute_b32 v50, v183, v91
	v_add_f32_e32 v52, v82, v86
	v_add_f32_e32 v53, v83, v87
	s_ashr_i32 s15, s14, 31
	s_or_b32 s36, s14, 1
	s_waitcnt lgkmcnt(0)
	v_add_f32_e32 v50, v91, v50
	ds_bpermute_b32 v51, v184, v50
	s_ashr_i32 s37, s36, 31
	s_or_b32 s34, s14, 2
	s_ashr_i32 s35, s34, 31
	s_or_b32 s30, s14, 3
	s_waitcnt lgkmcnt(0)
	v_add_f32_e32 v50, v50, v51
	v_fmamk_f32 v50, v50, 0x3a800000, v185
	v_mul_f32_e32 v51, 0x4f800000, v50
	v_cmp_gt_f32_e32 vcc, s39, v50
	s_ashr_i32 s31, s30, 31
	s_or_b32 s28, s14, 4
	v_cndmask_b32_e32 v50, v50, v51, vcc
	v_sqrt_f32_e32 v51, v50
	s_ashr_i32 s29, s28, 31
	s_or_b32 s26, s14, 5
	s_ashr_i32 s27, s26, 31
	v_add_u32_e32 v54, -1, v51
	v_add_u32_e32 v55, 1, v51
	v_fma_f32 v56, -v54, v51, v50
	v_fma_f32 v57, -v55, v51, v50
	v_cmp_ge_f32_e64 s[4:5], 0, v56
	s_or_b32 s24, s14, 6
	s_ashr_i32 s25, s24, 31
	v_cndmask_b32_e64 v51, v51, v54, s[4:5]
	v_cmp_lt_f32_e64 s[4:5], 0, v57
	s_or_b32 s22, s14, 7
	s_ashr_i32 s23, s22, 31
	v_cndmask_b32_e64 v51, v51, v55, s[4:5]
	v_mul_f32_e32 v54, 0x37800000, v51
	v_cndmask_b32_e32 v51, v51, v54, vcc
	v_cmp_class_f32_e32 vcc, v50, v186
	v_add_f32_e32 v55, v84, v88
	v_readlane_b32 s4, v255, 13
	v_cndmask_b32_e32 v50, v51, v50, vcc
	v_div_scale_f32 v51, s[2:3], v50, v50, 1.0
	v_rcp_f32_e32 v54, v51
	v_div_scale_f32 v56, vcc, 1.0, v50, 1.0
	v_readlane_b32 s5, v255, 14
	v_fma_f32 v57, -v51, v54, 1.0
	v_fmac_f32_e32 v54, v57, v54
	v_mul_f32_e32 v57, v56, v54
	v_fma_f32 v58, -v51, v57, v56
	v_fmac_f32_e32 v57, v58, v54
	v_fma_f32 v51, -v51, v57, v56
	v_div_fmas_f32 v51, v51, v54, v57
	v_div_fixup_f32 v181, v51, v50, 1.0
	v_add_f32_e32 v56, v85, v89
	v_mul_f32_e32 v54, v55, v181
	v_mul_f32_e32 v57, v56, v181
	v_mul_f32_e32 v50, v52, v181
	v_mul_f32_e32 v51, v53, v181
	v_max_f32_e32 v54, v54, v57
	v_max3_f32 v50, v50, v51, v54
	ds_bpermute_b32 v51, v183, v50
	s_ashr_i32 s2, s40, 9
	s_ashr_i32 s3, s2, 31
	v_readlane_b32 s33, v181, 0
	s_or_b32 s20, s14, 8
	s_waitcnt lgkmcnt(0)
	v_max_f32_e32 v51, v51, v51
	v_max_f32_e32 v50, v50, v51
	ds_bpermute_b32 v51, v184, v50
	v_mul_f32_e32 v206, s33, v2
	v_mul_f32_e32 v210, s33, v10
	s_ashr_i32 s21, s20, 31
	s_or_b32 s18, s14, 9
	s_waitcnt lgkmcnt(0)
	v_max_f32_e32 v51, v51, v51
	v_max_f32_e32 v50, v50, v51
	v_fma_f32 v51, v52, v181, -v50
	v_fma_f32 v52, v53, v181, -v50
	v_mul_f32_e32 v51, 0x3fb8aa3b, v51
	v_fma_f32 v53, v55, v181, -v50
	v_mul_f32_e32 v52, 0x3fb8aa3b, v52
	v_exp_f32_e32 v54, v51
	v_mul_f32_e32 v53, 0x3fb8aa3b, v53
	v_exp_f32_e32 v55, v52
	v_fma_f32 v50, v56, v181, -v50
	v_exp_f32_e32 v57, v53
	v_mul_f32_e32 v50, 0x3fb8aa3b, v50
	v_exp_f32_e32 v56, v50
	v_add_f32_e32 v50, 0, v54
	v_add_f32_e32 v50, v55, v50
	v_add_f32_e32 v50, v57, v50
	v_add_f32_e32 v50, v56, v50
	ds_bpermute_b32 v51, v183, v50
	s_ashr_i32 s19, s18, 31
	s_or_b32 s16, s14, 10
	s_ashr_i32 s17, s16, 31
	s_or_b32 s12, s14, 11
	s_waitcnt lgkmcnt(0)
	v_add_f32_e32 v52, v50, v51
	ds_bpermute_b32 v53, v184, v52
	v_and_b32_e32 v50, 0x1fff, v90
	v_lshlrev_b32_e32 v162, 2, v50
	v_lshl_add_u64 v[50:51], s[4:5], 0, v[162:163]
	s_ashr_i32 s13, s12, 31
	s_waitcnt lgkmcnt(0)
; __device__ __forceinline__ unsigned pk4_fp8(float a, float b, float c, float d) { unsigned w = 0u; w = __builtin_amdgcn_cvt_pk_fp8_f32(a, b, w, false); w = __builtin_amdgcn_cvt_pk_fp8_f32(c, d, w, true); return w; }
; __device__ __forceinline__ void unpack8(const v4u w, float (&y)[8]) { y[0] = bf_lo(w.x); y[1] = bf_hi(w.x); y[2] = bf_lo(w.y); y[3] = bf_hi(w.y); y[4] = bf_lo(w.z); y[5] = bf_hi(w.z); y[6] = bf_lo(w.w); y[7] = bf_hi(w.w); }
; __device__ __forceinline__ void norm_router_phase(const bf16* x1, const float* g, const float* Wr, unsigned char* XN8, float* AFF, LAS float* WT, int gw, int NGW, int lane, int tid, bool table_ready) {
;     ...
;         { const int row = row0 + ti; const float inv = 1.0f / sm;
; #pragma unroll
;           for (int r = 0; r < 4; ++r) AFF[((size_t)(4 * kq + r) * NB + (row >> 13)) * SEQ + (row & (SEQ - 1))] = ex[r] * inv; }
;         const unsigned rbits = __float_as_uint(rstd);
;         v4u xa[16], xb[16];
; #pragma unroll
;         for (int i = 0; i < 16; ++i) { const bf16* xr = x1 + (size_t)(row0 + i) * DM + 8 * lane; xa[i] = *(const v4u*)xr; xb[i] = *(const v4u*)(xr + 512); }
; #pragma unroll
;         for (int i = 0; i < 16; ++i) {
;             const float rs = __uint_as_float((unsigned)__builtin_amdgcn_readlane((int)rbits, i));
;             float v[16]; { float t[8]; unpack8(xa[i], t);
; #pragma unroll
;                 for (int j = 0; j < 8; ++j) v[j] = t[j] * (rs * gg[j]);
;                 unpack8(xb[i], t);
; #pragma unroll
;                 for (int j = 0; j < 8; ++j) v[8 + j] = t[j] * (rs * gg[8 + j]); }
;             unsigned char* o = XN8 + (size_t)(row0 + i) * DM + 8 * lane;
;             *(v2u*)o = (v2u){pg8::pk4_fp8(v[0], v[1], v[2], v[3]), pg8::pk4_fp8(v[4], v[5], v[6], v[7])};
;             *(v2u*)(o + 512) = (v2u){pg8::pk4_fp8(v[8], v[9], v[10], v[11]), pg8::pk4_fp8(v[12], v[13], v[14], v[15])};
	v_add_f32_e32 v58, v52, v53
	v_div_scale_f32 v59, s[4:5], v58, v58, 1.0
	v_rcp_f32_e32 v60, v59
	v_div_scale_f32 v61, vcc, 1.0, v58, 1.0
	v_lshl_add_u64 v[52:53], s[2:3], 0, v[164:165]
	v_fma_f32 v62, -v59, v60, 1.0
	v_fmac_f32_e32 v60, v62, v60
	v_mul_f32_e32 v62, v61, v60
	v_fma_f32 v63, -v59, v62, v61
	v_fmac_f32_e32 v62, v63, v60
	v_fma_f32 v59, -v59, v62, v61
	v_div_fmas_f32 v59, v59, v60, v62
	v_div_fixup_f32 v58, v59, v58, 1.0
	v_lshlrev_b64 v[52:53], 15, v[52:53]
	v_mul_f32_e32 v54, v54, v58
	v_lshl_add_u64 v[52:53], v[50:51], 0, v[52:53]
	global_store_dword v[52:53], v54, off
	v_lshl_add_u64 v[52:53], s[2:3], 0, v[172:173]
	v_lshlrev_b64 v[52:53], 15, v[52:53]
	v_mul_f32_e32 v54, v55, v58
	v_lshl_add_u64 v[52:53], v[50:51], 0, v[52:53]
	global_store_dword v[52:53], v54, off
	v_lshl_add_u64 v[52:53], s[2:3], 0, v[174:175]
	v_lshlrev_b64 v[52:53], 15, v[52:53]
	v_mul_f32_e32 v54, v57, v58
	v_lshl_add_u64 v[52:53], v[50:51], 0, v[52:53]
	global_store_dword v[52:53], v54, off
	v_lshl_add_u64 v[52:53], s[2:3], 0, v[176:177]
	v_lshlrev_b64 v[52:53], 15, v[52:53]
	v_mul_f32_e32 v54, v56, v58
	v_lshl_add_u64 v[50:51], v[50:51], 0, v[52:53]
	s_lshl_b64 s[2:3], s[14:15], 11
	global_store_dword v[50:51], v54, off
	v_lshl_add_u64 v[50:51], v[168:169], 0, s[2:3]
	s_nop 0
	s_nop 0
	s_lshl_b64 s[2:3], s[36:37], 11
	v_lshl_add_u64 v[50:51], v[168:169], 0, s[2:3]
	s_nop 0
	s_nop 0
	s_lshl_b64 s[2:3], s[34:35], 11
	v_lshl_add_u64 v[50:51], v[168:169], 0, s[2:3]
	s_nop 0
	s_nop 0
	s_lshl_b64 s[2:3], s[30:31], 11
	v_lshl_add_u64 v[50:51], v[168:169], 0, s[2:3]
	s_nop 0
	s_nop 0
	s_lshl_b64 s[2:3], s[28:29], 11
	v_lshl_add_u64 v[50:51], v[168:169], 0, s[2:3]
	s_lshl_b64 s[2:3], s[26:27], 11
	s_nop 0
	s_nop 0
	v_lshl_add_u64 v[50:51], v[168:169], 0, s[2:3]
	s_lshl_b64 s[2:3], s[24:25], 11
	s_nop 0
	s_nop 0
	v_lshl_add_u64 v[50:51], v[168:169], 0, s[2:3]
	s_lshl_b64 s[2:3], s[22:23], 11
	s_nop 0
	s_nop 0
	v_lshl_add_u64 v[50:51], v[168:169], 0, s[2:3]
	s_lshl_b64 s[2:3], s[20:21], 11
	s_nop 0
	s_nop 0
	v_lshl_add_u64 v[50:51], v[168:169], 0, s[2:3]
	s_lshl_b64 s[2:3], s[18:19], 11
	s_nop 0
	s_nop 0
	v_lshl_add_u64 v[50:51], v[168:169], 0, s[2:3]
	s_lshl_b64 s[2:3], s[16:17], 11
	s_or_b32 s10, s14, 12
	s_nop 0
	s_nop 0
	v_lshl_add_u64 v[50:51], v[168:169], 0, s[2:3]
	s_lshl_b64 s[2:3], s[12:13], 11
	s_ashr_i32 s11, s10, 31
	s_or_b32 s8, s14, 13
	global_load_dwordx4 v[94:97], v[50:51], off
	global_load_dwordx4 v[90:93], v[50:51], off offset:1024
	v_lshl_add_u64 v[50:51], v[168:169], 0, s[2:3]
	s_lshl_b64 s[2:3], s[10:11], 11
	s_ashr_i32 s9, s8, 31
	s_or_b32 s4, s14, 14
	global_load_dwordx4 v[86:89], v[50:51], off
	global_load_dwordx4 v[82:85], v[50:51], off offset:1024
	v_lshl_add_u64 v[50:51], v[168:169], 0, s[2:3]
	s_lshl_b64 s[2:3], s[8:9], 11
	s_ashr_i32 s5, s4, 31
	global_load_dwordx4 v[78:81], v[50:51], off
	global_load_dwordx4 v[74:77], v[50:51], off offset:1024
	v_lshl_add_u64 v[50:51], v[168:169], 0, s[2:3]
	s_lshl_b64 s[2:3], s[4:5], 11
	global_load_dwordx4 v[70:73], v[50:51], off
	global_load_dwordx4 v[66:69], v[50:51], off offset:1024
	v_lshl_add_u64 v[50:51], v[168:169], 0, s[2:3]
	s_or_b32 s2, s14, 15
	s_lshl_b64 s[14:15], s[14:15], 10
	s_ashr_i32 s3, s2, 31
	s_lshl_b64 s[42:43], s[2:3], 11
	global_load_dwordx4 v[62:65], v[50:51], off
	global_load_dwordx4 v[58:61], v[50:51], off offset:1024
	v_lshl_add_u64 v[50:51], v[168:169], 0, s[42:43]
	global_load_dwordx4 v[54:57], v[50:51], off
	s_nop 0
	global_load_dwordx4 v[50:53], v[50:51], off offset:1024
	s_lshl_b64 s[12:13], s[12:13], 10
	s_lshl_b64 s[10:11], s[10:11], 10
	s_lshl_b64 s[8:9], s[8:9], 10
	s_lshl_b64 s[4:5], s[4:5], 10
	s_lshl_b64 s[2:3], s[2:3], 10
	v_add_u32_e32 v180, s38, v180
	s_waitcnt vmcnt(31)
	v_lshlrev_b32_e32 v162, 16, v188
	v_and_b32_e32 v187, 0xffff0000, v188
	v_mul_f32_e32 v162, v206, v162
	v_mul_f32_e32 v206, s33, v3
	v_lshlrev_b32_e32 v188, 16, v189
	v_mul_f32_e32 v187, v206, v187
	v_mul_f32_e32 v206, s33, v4
	v_and_b32_e32 v189, 0xffff0000, v189
	v_mul_f32_e32 v206, v206, v188
	v_mul_f32_e32 v188, s33, v5
	v_lshlrev_b32_e32 v204, 16, v190
	v_mul_f32_e32 v207, v188, v189
	v_mul_f32_e32 v188, s33, v6
	v_and_b32_e32 v190, 0xffff0000, v190
	v_mul_f32_e32 v204, v188, v204
	v_mul_f32_e32 v188, s33, v7
	v_lshlrev_b32_e32 v205, 16, v191
	v_mul_f32_e32 v190, v188, v190
	v_mul_f32_e32 v188, s33, v8
	v_and_b32_e32 v191, 0xffff0000, v191
	v_mul_f32_e32 v205, v188, v205
	v_mul_f32_e32 v188, s33, v9
	v_mul_f32_e32 v208, v188, v191
	s_waitcnt vmcnt(30)
	v_lshlrev_b32_e32 v188, 16, v192
	v_and_b32_e32 v189, 0xffff0000, v192
	v_mul_f32_e32 v210, v210, v188
	v_mul_f32_e32 v188, s33, v11
	v_lshlrev_b32_e32 v191, 16, v193
	v_mul_f32_e32 v211, v188, v189
	v_mul_f32_e32 v188, s33, v12
	v_and_b32_e32 v192, 0xffff0000, v193
	v_mul_f32_e32 v212, v188, v191
	v_mul_f32_e32 v188, s33, v13
	v_lshlrev_b32_e32 v193, 16, v194
	v_mul_f32_e32 v192, v188, v192
	v_mul_f32_e32 v188, s33, v14
	v_and_b32_e32 v194, 0xffff0000, v194
	v_mul_f32_e32 v193, v188, v193
	v_mul_f32_e32 v188, s33, v15
	v_lshlrev_b32_e32 v209, 16, v195
	v_mul_f32_e32 v194, v188, v194
	v_mul_f32_e32 v188, s33, v16
	v_and_b32_e32 v195, 0xffff0000, v195
	v_mul_f32_e32 v209, v188, v209
	v_mul_f32_e32 v188, s33, v17
	v_mul_f32_e32 v195, v188, v195
	v_mov_b32_e32 v188, v163
	v_mov_b32_e32 v189, v163
	v_cvt_pk_fp8_f32 v188, v162, v187
	v_cvt_pk_fp8_f32 v189, v204, v190
	v_mov_b32_e32 v190, v163
	v_mov_b32_e32 v191, v163
	v_cvt_pk_fp8_f32 v190, v210, v211
	v_cvt_pk_fp8_f32 v191, v193, v194
	v_cvt_pk_fp8_f32 v188, v206, v207 op_sel:[0,0,1]
	v_cvt_pk_fp8_f32 v189, v205, v208 op_sel:[0,0,1]
	v_cvt_pk_fp8_f32 v190, v212, v192 op_sel:[0,0,1]
	v_cvt_pk_fp8_f32 v191, v209, v195 op_sel:[0,0,1]
	v_lshl_add_u64 v[192:193], v[170:171], 0, s[14:15]
	v_readlane_b32 s14, v181, 1
	s_waitcnt vmcnt(29)
; __device__ __forceinline__ unsigned pk4_fp8(float a, float b, float c, float d) { unsigned w = 0u; w = __builtin_amdgcn_cvt_pk_fp8_f32(a, b, w, false); w = __builtin_amdgcn_cvt_pk_fp8_f32(c, d, w, true); return w; }
; __device__ __forceinline__ void unpack8(const v4u w, float (&y)[8]) { y[0] = bf_lo(w.x); y[1] = bf_hi(w.x); y[2] = bf_lo(w.y); y[3] = bf_hi(w.y); y[4] = bf_lo(w.z); y[5] = bf_hi(w.z); y[6] = bf_lo(w.w); y[7] = bf_hi(w.w); }
; __device__ __forceinline__ void norm_router_phase(const bf16* x1, const float* g, const float* Wr, unsigned char* XN8, float* AFF, LAS float* WT, int gw, int NGW, int lane, int tid, bool table_ready) {
;     ...
;         for (int i = 0; i < 16; ++i) { const bf16* xr = x1 + (size_t)(row0 + i) * DM + 8 * lane; xa[i] = *(const v4u*)xr; xb[i] = *(const v4u*)(xr + 512); }
; #pragma unroll
;         for (int i = 0; i < 16; ++i) {
;             const float rs = __uint_as_float((unsigned)__builtin_amdgcn_readlane((int)rbits, i));
;             float v[16]; { float t[8]; unpack8(xa[i], t);
; #pragma unroll
;                 for (int j = 0; j < 8; ++j) v[j] = t[j] * (rs * gg[j]);
;                 unpack8(xb[i], t);
; #pragma unroll
;                 for (int j = 0; j < 8; ++j) v[8 + j] = t[j] * (rs * gg[8 + j]); }
;             unsigned char* o = XN8 + (size_t)(row0 + i) * DM + 8 * lane;
;             *(v2u*)o = (v2u){pg8::pk4_fp8(v[0], v[1], v[2], v[3]), pg8::pk4_fp8(v[4], v[5], v[6], v[7])};
;             *(v2u*)(o + 512) = (v2u){pg8::pk4_fp8(v[8], v[9], v[10], v[11]), pg8::pk4_fp8(v[12], v[13], v[14], v[15])};
;         }
	v_lshlrev_b32_e32 v162, 16, v196
	v_and_b32_e32 v187, 0xffff0000, v196
	v_mul_f32_e32 v194, s14, v2
	v_mul_f32_e32 v162, v194, v162
	v_mul_f32_e32 v194, s14, v3
	global_store_dwordx2 v[192:193], v[188:189], off
	global_store_dwordx2 v[192:193], v[190:191], off offset:512
	v_lshlrev_b32_e32 v188, 16, v197
	v_mul_f32_e32 v187, v194, v187
	v_mul_f32_e32 v194, s14, v4
	v_and_b32_e32 v189, 0xffff0000, v197
	v_mul_f32_e32 v194, v194, v188
	v_mul_f32_e32 v188, s14, v5
	v_lshlrev_b32_e32 v190, 16, v198
	v_mul_f32_e32 v195, v188, v189
	v_mul_f32_e32 v188, s14, v6
	v_and_b32_e32 v191, 0xffff0000, v198
	v_mul_f32_e32 v190, v188, v190
	v_mul_f32_e32 v188, s14, v7
	v_lshlrev_b32_e32 v192, 16, v199
	v_mul_f32_e32 v191, v188, v191
	v_mul_f32_e32 v188, s14, v8
	v_and_b32_e32 v193, 0xffff0000, v199
	v_mul_f32_e32 v192, v188, v192
	v_mul_f32_e32 v188, s14, v9
	v_mul_f32_e32 v193, v188, v193
	s_waitcnt vmcnt(30)
	v_lshlrev_b32_e32 v188, 16, v200
	v_lshlrev_b32_e32 v198, 16, v202
	v_and_b32_e32 v199, 0xffff0000, v202
	v_mul_f32_e32 v202, s14, v10
	v_and_b32_e32 v189, 0xffff0000, v200
	v_mul_f32_e32 v202, v202, v188
	v_mul_f32_e32 v188, s14, v11
	v_lshlrev_b32_e32 v196, 16, v201
	v_and_b32_e32 v197, 0xffff0000, v201
	v_lshlrev_b32_e32 v200, 16, v203
	v_and_b32_e32 v201, 0xffff0000, v203
	v_mul_f32_e32 v203, v188, v189
	v_mul_f32_e32 v188, s14, v12
	v_mul_f32_e32 v196, v188, v196
	v_mul_f32_e32 v188, s14, v13
	v_mul_f32_e32 v197, v188, v197
	v_mul_f32_e32 v188, s14, v14
	v_mul_f32_e32 v198, v188, v198
	v_mul_f32_e32 v188, s14, v15
	v_mul_f32_e32 v199, v188, v199
	v_mul_f32_e32 v188, s14, v16
	v_mul_f32_e32 v200, v188, v200
	v_mul_f32_e32 v188, s14, v17
	v_mul_f32_e32 v201, v188, v201
	v_mov_b32_e32 v188, v163
	v_mov_b32_e32 v189, v163
	v_cvt_pk_fp8_f32 v188, v162, v187
	v_cvt_pk_fp8_f32 v189, v190, v191
	v_mov_b32_e32 v190, v163
	v_mov_b32_e32 v191, v163
	v_cvt_pk_fp8_f32 v190, v202, v203
	v_cvt_pk_fp8_f32 v191, v198, v199
	v_cvt_pk_fp8_f32 v188, v194, v195 op_sel:[0,0,1]
	v_cvt_pk_fp8_f32 v189, v192, v193 op_sel:[0,0,1]
	v_cvt_pk_fp8_f32 v190, v196, v197 op_sel:[0,0,1]
	v_cvt_pk_fp8_f32 v191, v200, v201 op_sel:[0,0,1]
	s_lshl_b64 s[14:15], s[36:37], 10
	v_lshl_add_u64 v[192:193], v[170:171], 0, s[14:15]
	v_readlane_b32 s14, v181, 2
	global_store_dwordx2 v[192:193], v[188:189], off
	global_store_dwordx2 v[192:193], v[190:191], off offset:512
	s_waitcnt vmcnt(31)
	v_lshlrev_b32_e32 v162, 16, v158
	v_mul_f32_e32 v190, s14, v2
	v_and_b32_e32 v158, 0xffff0000, v158
	v_mul_f32_e32 v162, v190, v162
	v_mul_f32_e32 v190, s14, v3
	v_lshlrev_b32_e32 v187, 16, v159
	v_mul_f32_e32 v158, v190, v158
	v_mul_f32_e32 v190, s14, v4
	v_and_b32_e32 v159, 0xffff0000, v159
	v_mul_f32_e32 v187, v190, v187
	v_mul_f32_e32 v190, s14, v5
	v_lshlrev_b32_e32 v188, 16, v160
	v_mul_f32_e32 v159, v190, v159
	v_mul_f32_e32 v190, s14, v6
	v_and_b32_e32 v160, 0xffff0000, v160
	v_mul_f32_e32 v188, v190, v188
	v_mul_f32_e32 v190, s14, v7
	v_lshlrev_b32_e32 v189, 16, v161
	v_mul_f32_e32 v160, v190, v160
	v_mul_f32_e32 v190, s14, v8
	v_and_b32_e32 v161, 0xffff0000, v161
	v_mul_f32_e32 v189, v190, v189
	v_mul_f32_e32 v190, s14, v9
	v_mul_f32_e32 v161, v190, v161
	s_waitcnt vmcnt(30)
	v_lshlrev_b32_e32 v190, 16, v154
	v_mul_f32_e32 v194, s14, v10
	v_and_b32_e32 v154, 0xffff0000, v154
	v_mul_f32_e32 v190, v194, v190
	v_mul_f32_e32 v194, s14, v11
	v_lshlrev_b32_e32 v191, 16, v155
	v_mul_f32_e32 v194, v194, v154
	v_mul_f32_e32 v154, s14, v12
	v_and_b32_e32 v155, 0xffff0000, v155
	v_mul_f32_e32 v191, v154, v191
	v_mul_f32_e32 v154, s14, v13
	v_lshlrev_b32_e32 v192, 16, v156
	v_mul_f32_e32 v195, v154, v155
	v_mul_f32_e32 v154, s14, v14
	v_and_b32_e32 v156, 0xffff0000, v156
	v_mul_f32_e32 v192, v154, v192
	v_mul_f32_e32 v154, s14, v15
	v_lshlrev_b32_e32 v193, 16, v157
	v_mul_f32_e32 v196, v154, v156
	v_mul_f32_e32 v154, s14, v16
	v_and_b32_e32 v157, 0xffff0000, v157
	v_mul_f32_e32 v193, v154, v193
	v_mul_f32_e32 v154, s14, v17
	v_mul_f32_e32 v197, v154, v157
	v_mov_b32_e32 v154, v163
	v_mov_b32_e32 v155, v163
	v_cvt_pk_fp8_f32 v154, v162, v158
	v_cvt_pk_fp8_f32 v155, v188, v160
	v_mov_b32_e32 v156, v163
	v_mov_b32_e32 v157, v163
	v_cvt_pk_fp8_f32 v156, v190, v194
	v_cvt_pk_fp8_f32 v157, v192, v196
	v_cvt_pk_fp8_f32 v154, v187, v159 op_sel:[0,0,1]
	v_cvt_pk_fp8_f32 v155, v189, v161 op_sel:[0,0,1]
	v_cvt_pk_fp8_f32 v156, v191, v195 op_sel:[0,0,1]
	v_cvt_pk_fp8_f32 v157, v193, v197 op_sel:[0,0,1]
	s_lshl_b64 s[14:15], s[34:35], 10
	v_lshl_add_u64 v[158:159], v[170:171], 0, s[14:15]
	v_readlane_b32 s14, v181, 3
	global_store_dwordx2 v[158:159], v[154:155], off
	global_store_dwordx2 v[158:159], v[156:157], off offset:512
	s_waitcnt vmcnt(31)
	v_lshlrev_b32_e32 v154, 16, v150
	v_mul_f32_e32 v158, s14, v2
	v_and_b32_e32 v150, 0xffff0000, v150
	v_mul_f32_e32 v154, v158, v154
	v_mul_f32_e32 v158, s14, v3
	v_lshlrev_b32_e32 v155, 16, v151
	v_mul_f32_e32 v150, v158, v150
	v_mul_f32_e32 v158, s14, v4
	v_and_b32_e32 v151, 0xffff0000, v151
	v_mul_f32_e32 v155, v158, v155
	v_mul_f32_e32 v158, s14, v5
	v_lshlrev_b32_e32 v156, 16, v152
	v_mul_f32_e32 v151, v158, v151
	v_mul_f32_e32 v158, s14, v6
	v_and_b32_e32 v152, 0xffff0000, v152
	v_mul_f32_e32 v156, v158, v156
	v_mul_f32_e32 v158, s14, v7
	v_lshlrev_b32_e32 v157, 16, v153
	v_mul_f32_e32 v152, v158, v152
	v_mul_f32_e32 v158, s14, v8
	v_and_b32_e32 v153, 0xffff0000, v153
	v_mul_f32_e32 v157, v158, v157
	v_mul_f32_e32 v158, s14, v9
	v_mul_f32_e32 v153, v158, v153
	s_waitcnt vmcnt(30)
; __device__ __forceinline__ unsigned pk4_fp8(float a, float b, float c, float d) { unsigned w = 0u; w = __builtin_amdgcn_cvt_pk_fp8_f32(a, b, w, false); w = __builtin_amdgcn_cvt_pk_fp8_f32(c, d, w, true); return w; }
; __device__ __forceinline__ void unpack8(const v4u w, float (&y)[8]) { y[0] = bf_lo(w.x); y[1] = bf_hi(w.x); y[2] = bf_lo(w.y); y[3] = bf_hi(w.y); y[4] = bf_lo(w.z); y[5] = bf_hi(w.z); y[6] = bf_lo(w.w); y[7] = bf_hi(w.w); }
; __device__ __forceinline__ void norm_router_phase(const bf16* x1, const float* g, const float* Wr, unsigned char* XN8, float* AFF, LAS float* WT, int gw, int NGW, int lane, int tid, bool table_ready) {
;     ...
;         for (int i = 0; i < 16; ++i) { const bf16* xr = x1 + (size_t)(row0 + i) * DM + 8 * lane; xa[i] = *(const v4u*)xr; xb[i] = *(const v4u*)(xr + 512); }
; #pragma unroll
;         for (int i = 0; i < 16; ++i) {
;             const float rs = __uint_as_float((unsigned)__builtin_amdgcn_readlane((int)rbits, i));
;             float v[16]; { float t[8]; unpack8(xa[i], t);
; #pragma unroll
;                 for (int j = 0; j < 8; ++j) v[j] = t[j] * (rs * gg[j]);
;                 unpack8(xb[i], t);
; #pragma unroll
;                 for (int j = 0; j < 8; ++j) v[8 + j] = t[j] * (rs * gg[8 + j]); }
;             unsigned char* o = XN8 + (size_t)(row0 + i) * DM + 8 * lane;
;             *(v2u*)o = (v2u){pg8::pk4_fp8(v[0], v[1], v[2], v[3]), pg8::pk4_fp8(v[4], v[5], v[6], v[7])};
;             *(v2u*)(o + 512) = (v2u){pg8::pk4_fp8(v[8], v[9], v[10], v[11]), pg8::pk4_fp8(v[12], v[13], v[14], v[15])};
;         }
	v_lshlrev_b32_e32 v158, 16, v146
	v_mul_f32_e32 v162, s14, v10
	v_and_b32_e32 v146, 0xffff0000, v146
	v_mul_f32_e32 v158, v162, v158
	v_mul_f32_e32 v162, s14, v11
	v_lshlrev_b32_e32 v159, 16, v147
	v_mul_f32_e32 v162, v162, v146
	v_mul_f32_e32 v146, s14, v12
	v_and_b32_e32 v147, 0xffff0000, v147
	v_mul_f32_e32 v159, v146, v159
	v_mul_f32_e32 v146, s14, v13
	v_lshlrev_b32_e32 v160, 16, v148
	v_mul_f32_e32 v187, v146, v147
	v_mul_f32_e32 v146, s14, v14
	v_and_b32_e32 v148, 0xffff0000, v148
	v_mul_f32_e32 v160, v146, v160
	v_mul_f32_e32 v146, s14, v15
	v_lshlrev_b32_e32 v161, 16, v149
	v_mul_f32_e32 v188, v146, v148
	v_mul_f32_e32 v146, s14, v16
	v_and_b32_e32 v149, 0xffff0000, v149
	v_mul_f32_e32 v161, v146, v161
	v_mul_f32_e32 v146, s14, v17
	v_mul_f32_e32 v189, v146, v149
	v_mov_b32_e32 v146, v163
	v_mov_b32_e32 v147, v163
	v_cvt_pk_fp8_f32 v146, v154, v150
	v_cvt_pk_fp8_f32 v147, v156, v152
	v_mov_b32_e32 v148, v163
	v_mov_b32_e32 v149, v163
	v_cvt_pk_fp8_f32 v148, v158, v162
	v_cvt_pk_fp8_f32 v149, v160, v188
	v_cvt_pk_fp8_f32 v146, v155, v151 op_sel:[0,0,1]
	v_cvt_pk_fp8_f32 v147, v157, v153 op_sel:[0,0,1]
	v_cvt_pk_fp8_f32 v148, v159, v187 op_sel:[0,0,1]
	v_cvt_pk_fp8_f32 v149, v161, v189 op_sel:[0,0,1]
	s_lshl_b64 s[14:15], s[30:31], 10
	v_lshl_add_u64 v[150:151], v[170:171], 0, s[14:15]
	v_readlane_b32 s14, v181, 4
	global_store_dwordx2 v[150:151], v[146:147], off
	global_store_dwordx2 v[150:151], v[148:149], off offset:512
	s_waitcnt vmcnt(31)
	v_lshlrev_b32_e32 v146, 16, v142
	v_mul_f32_e32 v150, s14, v2
	v_and_b32_e32 v142, 0xffff0000, v142
	v_mul_f32_e32 v146, v150, v146
	v_mul_f32_e32 v150, s14, v3
	v_lshlrev_b32_e32 v147, 16, v143
	v_mul_f32_e32 v142, v150, v142
	v_mul_f32_e32 v150, s14, v4
	v_and_b32_e32 v143, 0xffff0000, v143
	v_mul_f32_e32 v147, v150, v147
	v_mul_f32_e32 v150, s14, v5
	v_lshlrev_b32_e32 v148, 16, v144
	v_mul_f32_e32 v143, v150, v143
	v_mul_f32_e32 v150, s14, v6
	v_and_b32_e32 v144, 0xffff0000, v144
	v_mul_f32_e32 v148, v150, v148
	v_mul_f32_e32 v150, s14, v7
	v_lshlrev_b32_e32 v149, 16, v145
	v_mul_f32_e32 v144, v150, v144
	v_mul_f32_e32 v150, s14, v8
	v_and_b32_e32 v145, 0xffff0000, v145
	v_mul_f32_e32 v149, v150, v149
	v_mul_f32_e32 v150, s14, v9
	v_mul_f32_e32 v145, v150, v145
	s_waitcnt vmcnt(30)
	v_lshlrev_b32_e32 v150, 16, v138
	v_mul_f32_e32 v154, s14, v10
	v_and_b32_e32 v138, 0xffff0000, v138
	v_mul_f32_e32 v150, v154, v150
	v_mul_f32_e32 v154, s14, v11
	v_lshlrev_b32_e32 v151, 16, v139
	v_mul_f32_e32 v154, v154, v138
	v_mul_f32_e32 v138, s14, v12
	v_and_b32_e32 v139, 0xffff0000, v139
	v_mul_f32_e32 v151, v138, v151
	v_mul_f32_e32 v138, s14, v13
	v_lshlrev_b32_e32 v152, 16, v140
	v_mul_f32_e32 v155, v138, v139
	v_mul_f32_e32 v138, s14, v14
	v_and_b32_e32 v140, 0xffff0000, v140
	v_mul_f32_e32 v152, v138, v152
	v_mul_f32_e32 v138, s14, v15
	v_lshlrev_b32_e32 v153, 16, v141
	v_mul_f32_e32 v156, v138, v140
	v_mul_f32_e32 v138, s14, v16
	v_and_b32_e32 v141, 0xffff0000, v141
	v_mul_f32_e32 v153, v138, v153
	v_mul_f32_e32 v138, s14, v17
	v_mul_f32_e32 v157, v138, v141
	v_mov_b32_e32 v138, v163
	v_mov_b32_e32 v139, v163
	v_cvt_pk_fp8_f32 v138, v146, v142
	v_cvt_pk_fp8_f32 v139, v148, v144
	v_mov_b32_e32 v140, v163
	v_mov_b32_e32 v141, v163
	v_cvt_pk_fp8_f32 v140, v150, v154
	v_cvt_pk_fp8_f32 v141, v152, v156
	v_cvt_pk_fp8_f32 v138, v147, v143 op_sel:[0,0,1]
	v_cvt_pk_fp8_f32 v139, v149, v145 op_sel:[0,0,1]
	v_cvt_pk_fp8_f32 v140, v151, v155 op_sel:[0,0,1]
	v_cvt_pk_fp8_f32 v141, v153, v157 op_sel:[0,0,1]
	s_lshl_b64 s[14:15], s[28:29], 10
	v_lshl_add_u64 v[142:143], v[170:171], 0, s[14:15]
	v_readlane_b32 s14, v181, 5
	global_store_dwordx2 v[142:143], v[138:139], off
	global_store_dwordx2 v[142:143], v[140:141], off offset:512
	s_waitcnt vmcnt(31)
	v_lshlrev_b32_e32 v138, 16, v134
	v_mul_f32_e32 v142, s14, v2
	v_and_b32_e32 v134, 0xffff0000, v134
	v_mul_f32_e32 v138, v142, v138
	v_mul_f32_e32 v142, s14, v3
	v_lshlrev_b32_e32 v139, 16, v135
	v_mul_f32_e32 v134, v142, v134
	v_mul_f32_e32 v142, s14, v4
	v_and_b32_e32 v135, 0xffff0000, v135
	v_mul_f32_e32 v139, v142, v139
	v_mul_f32_e32 v142, s14, v5
	v_lshlrev_b32_e32 v140, 16, v136
	v_mul_f32_e32 v135, v142, v135
	v_mul_f32_e32 v142, s14, v6
	v_and_b32_e32 v136, 0xffff0000, v136
	v_mul_f32_e32 v140, v142, v140
	v_mul_f32_e32 v142, s14, v7
	v_lshlrev_b32_e32 v141, 16, v137
	v_mul_f32_e32 v136, v142, v136
	v_mul_f32_e32 v142, s14, v8
	v_and_b32_e32 v137, 0xffff0000, v137
	v_mul_f32_e32 v141, v142, v141
	v_mul_f32_e32 v142, s14, v9
	v_mul_f32_e32 v137, v142, v137
	s_waitcnt vmcnt(30)
	v_lshlrev_b32_e32 v142, 16, v130
	v_mul_f32_e32 v146, s14, v10
	v_and_b32_e32 v130, 0xffff0000, v130
	v_mul_f32_e32 v142, v146, v142
	v_mul_f32_e32 v146, s14, v11
	v_lshlrev_b32_e32 v143, 16, v131
	v_mul_f32_e32 v146, v146, v130
	v_mul_f32_e32 v130, s14, v12
	v_and_b32_e32 v131, 0xffff0000, v131
	v_mul_f32_e32 v143, v130, v143
	v_mul_f32_e32 v130, s14, v13
	v_lshlrev_b32_e32 v144, 16, v132
	v_mul_f32_e32 v147, v130, v131
	v_mul_f32_e32 v130, s14, v14
	v_and_b32_e32 v132, 0xffff0000, v132
	v_mul_f32_e32 v144, v130, v144
	v_mul_f32_e32 v130, s14, v15
	v_lshlrev_b32_e32 v145, 16, v133
	v_mul_f32_e32 v148, v130, v132
	v_mul_f32_e32 v130, s14, v16
	v_and_b32_e32 v133, 0xffff0000, v133
	v_mul_f32_e32 v145, v130, v145
	v_mul_f32_e32 v130, s14, v17
	v_mul_f32_e32 v149, v130, v133
	v_mov_b32_e32 v130, v163
	v_mov_b32_e32 v131, v163
	v_cvt_pk_fp8_f32 v130, v138, v134
	v_cvt_pk_fp8_f32 v131, v140, v136
	v_mov_b32_e32 v132, v163
	v_mov_b32_e32 v133, v163
	v_cvt_pk_fp8_f32 v132, v142, v146
	v_cvt_pk_fp8_f32 v133, v144, v148
	v_cvt_pk_fp8_f32 v130, v139, v135 op_sel:[0,0,1]
	v_cvt_pk_fp8_f32 v131, v141, v137 op_sel:[0,0,1]
	v_cvt_pk_fp8_f32 v132, v143, v147 op_sel:[0,0,1]
	v_cvt_pk_fp8_f32 v133, v145, v149 op_sel:[0,0,1]
	s_lshl_b64 s[14:15], s[26:27], 10
	v_lshl_add_u64 v[134:135], v[170:171], 0, s[14:15]
	v_readlane_b32 s14, v181, 6
	global_store_dwordx2 v[134:135], v[130:131], off
	global_store_dwordx2 v[134:135], v[132:133], off offset:512
	s_waitcnt vmcnt(31)
; __device__ __forceinline__ unsigned pk4_fp8(float a, float b, float c, float d) { unsigned w = 0u; w = __builtin_amdgcn_cvt_pk_fp8_f32(a, b, w, false); w = __builtin_amdgcn_cvt_pk_fp8_f32(c, d, w, true); return w; }
; __device__ __forceinline__ void unpack8(const v4u w, float (&y)[8]) { y[0] = bf_lo(w.x); y[1] = bf_hi(w.x); y[2] = bf_lo(w.y); y[3] = bf_hi(w.y); y[4] = bf_lo(w.z); y[5] = bf_hi(w.z); y[6] = bf_lo(w.w); y[7] = bf_hi(w.w); }
; __device__ __forceinline__ void norm_router_phase(const bf16* x1, const float* g, const float* Wr, unsigned char* XN8, float* AFF, LAS float* WT, int gw, int NGW, int lane, int tid, bool table_ready) {
;     ...
;         for (int i = 0; i < 16; ++i) { const bf16* xr = x1 + (size_t)(row0 + i) * DM + 8 * lane; xa[i] = *(const v4u*)xr; xb[i] = *(const v4u*)(xr + 512); }
; #pragma unroll
;         for (int i = 0; i < 16; ++i) {
;             const float rs = __uint_as_float((unsigned)__builtin_amdgcn_readlane((int)rbits, i));
;             float v[16]; { float t[8]; unpack8(xa[i], t);
; #pragma unroll
;                 for (int j = 0; j < 8; ++j) v[j] = t[j] * (rs * gg[j]);
;                 unpack8(xb[i], t);
; #pragma unroll
;                 for (int j = 0; j < 8; ++j) v[8 + j] = t[j] * (rs * gg[8 + j]); }
;             unsigned char* o = XN8 + (size_t)(row0 + i) * DM + 8 * lane;
;             *(v2u*)o = (v2u){pg8::pk4_fp8(v[0], v[1], v[2], v[3]), pg8::pk4_fp8(v[4], v[5], v[6], v[7])};
;             *(v2u*)(o + 512) = (v2u){pg8::pk4_fp8(v[8], v[9], v[10], v[11]), pg8::pk4_fp8(v[12], v[13], v[14], v[15])};
;         }
	v_lshlrev_b32_e32 v130, 16, v126
	v_mul_f32_e32 v134, s14, v2
	v_and_b32_e32 v126, 0xffff0000, v126
	v_mul_f32_e32 v130, v134, v130
	v_mul_f32_e32 v134, s14, v3
	v_lshlrev_b32_e32 v131, 16, v127
	v_mul_f32_e32 v126, v134, v126
	v_mul_f32_e32 v134, s14, v4
	v_and_b32_e32 v127, 0xffff0000, v127
	v_mul_f32_e32 v131, v134, v131
	v_mul_f32_e32 v134, s14, v5
	v_lshlrev_b32_e32 v132, 16, v128
	v_mul_f32_e32 v127, v134, v127
	v_mul_f32_e32 v134, s14, v6
	v_and_b32_e32 v128, 0xffff0000, v128
	v_mul_f32_e32 v132, v134, v132
	v_mul_f32_e32 v134, s14, v7
	v_lshlrev_b32_e32 v133, 16, v129
	v_mul_f32_e32 v128, v134, v128
	v_mul_f32_e32 v134, s14, v8
	v_and_b32_e32 v129, 0xffff0000, v129
	v_mul_f32_e32 v133, v134, v133
	v_mul_f32_e32 v134, s14, v9
	v_mul_f32_e32 v129, v134, v129
	s_waitcnt vmcnt(30)
	v_lshlrev_b32_e32 v134, 16, v122
	v_mul_f32_e32 v138, s14, v10
	v_and_b32_e32 v122, 0xffff0000, v122
	v_mul_f32_e32 v134, v138, v134
	v_mul_f32_e32 v138, s14, v11
	v_lshlrev_b32_e32 v135, 16, v123
	v_mul_f32_e32 v138, v138, v122
	v_mul_f32_e32 v122, s14, v12
	v_and_b32_e32 v123, 0xffff0000, v123
	v_mul_f32_e32 v135, v122, v135
	v_mul_f32_e32 v122, s14, v13
	v_lshlrev_b32_e32 v136, 16, v124
	v_mul_f32_e32 v139, v122, v123
	v_mul_f32_e32 v122, s14, v14
	v_and_b32_e32 v124, 0xffff0000, v124
	v_mul_f32_e32 v136, v122, v136
	v_mul_f32_e32 v122, s14, v15
	v_lshlrev_b32_e32 v137, 16, v125
	v_mul_f32_e32 v140, v122, v124
	v_mul_f32_e32 v122, s14, v16
	v_and_b32_e32 v125, 0xffff0000, v125
	v_mul_f32_e32 v137, v122, v137
	v_mul_f32_e32 v122, s14, v17
	v_mul_f32_e32 v141, v122, v125
	v_mov_b32_e32 v122, v163
	v_mov_b32_e32 v123, v163
	v_cvt_pk_fp8_f32 v122, v130, v126
	v_cvt_pk_fp8_f32 v123, v132, v128
	v_mov_b32_e32 v124, v163
	v_mov_b32_e32 v125, v163
	v_cvt_pk_fp8_f32 v124, v134, v138
	v_cvt_pk_fp8_f32 v125, v136, v140
	v_cvt_pk_fp8_f32 v122, v131, v127 op_sel:[0,0,1]
	v_cvt_pk_fp8_f32 v123, v133, v129 op_sel:[0,0,1]
	v_cvt_pk_fp8_f32 v124, v135, v139 op_sel:[0,0,1]
	v_cvt_pk_fp8_f32 v125, v137, v141 op_sel:[0,0,1]
	s_lshl_b64 s[14:15], s[24:25], 10
	v_lshl_add_u64 v[126:127], v[170:171], 0, s[14:15]
	v_readlane_b32 s14, v181, 7
	global_store_dwordx2 v[126:127], v[122:123], off
	global_store_dwordx2 v[126:127], v[124:125], off offset:512
	s_waitcnt vmcnt(31)
	v_lshlrev_b32_e32 v122, 16, v118
	v_mul_f32_e32 v126, s14, v2
	v_and_b32_e32 v118, 0xffff0000, v118
	v_mul_f32_e32 v122, v126, v122
	v_mul_f32_e32 v126, s14, v3
	v_lshlrev_b32_e32 v123, 16, v119
	v_mul_f32_e32 v118, v126, v118
	v_mul_f32_e32 v126, s14, v4
	v_and_b32_e32 v119, 0xffff0000, v119
	v_mul_f32_e32 v123, v126, v123
	v_mul_f32_e32 v126, s14, v5
	v_lshlrev_b32_e32 v124, 16, v120
	v_mul_f32_e32 v119, v126, v119
	v_mul_f32_e32 v126, s14, v6
	v_and_b32_e32 v120, 0xffff0000, v120
	v_mul_f32_e32 v124, v126, v124
	v_mul_f32_e32 v126, s14, v7
	v_lshlrev_b32_e32 v125, 16, v121
	v_mul_f32_e32 v120, v126, v120
	v_mul_f32_e32 v126, s14, v8
	v_and_b32_e32 v121, 0xffff0000, v121
	v_mul_f32_e32 v125, v126, v125
	v_mul_f32_e32 v126, s14, v9
	v_mul_f32_e32 v121, v126, v121
	s_waitcnt vmcnt(30)
	v_lshlrev_b32_e32 v126, 16, v114
	v_mul_f32_e32 v130, s14, v10
	v_and_b32_e32 v114, 0xffff0000, v114
	v_mul_f32_e32 v126, v130, v126
	v_mul_f32_e32 v130, s14, v11
	v_lshlrev_b32_e32 v127, 16, v115
	v_mul_f32_e32 v130, v130, v114
	v_mul_f32_e32 v114, s14, v12
	v_and_b32_e32 v115, 0xffff0000, v115
	v_mul_f32_e32 v127, v114, v127
	v_mul_f32_e32 v114, s14, v13
	v_lshlrev_b32_e32 v128, 16, v116
	v_mul_f32_e32 v131, v114, v115
	v_mul_f32_e32 v114, s14, v14
	v_and_b32_e32 v116, 0xffff0000, v116
	v_mul_f32_e32 v128, v114, v128
	v_mul_f32_e32 v114, s14, v15
	v_lshlrev_b32_e32 v129, 16, v117
	v_mul_f32_e32 v132, v114, v116
	v_mul_f32_e32 v114, s14, v16
	v_and_b32_e32 v117, 0xffff0000, v117
	v_mul_f32_e32 v129, v114, v129
	v_mul_f32_e32 v114, s14, v17
	v_mul_f32_e32 v133, v114, v117
	v_mov_b32_e32 v114, v163
	v_mov_b32_e32 v115, v163
	v_cvt_pk_fp8_f32 v114, v122, v118
	v_cvt_pk_fp8_f32 v115, v124, v120
	v_mov_b32_e32 v116, v163
	v_mov_b32_e32 v117, v163
	v_cvt_pk_fp8_f32 v116, v126, v130
	v_cvt_pk_fp8_f32 v117, v128, v132
	v_cvt_pk_fp8_f32 v114, v123, v119 op_sel:[0,0,1]
	v_cvt_pk_fp8_f32 v115, v125, v121 op_sel:[0,0,1]
	v_cvt_pk_fp8_f32 v116, v127, v131 op_sel:[0,0,1]
	v_cvt_pk_fp8_f32 v117, v129, v133 op_sel:[0,0,1]
	s_lshl_b64 s[14:15], s[22:23], 10
	v_lshl_add_u64 v[118:119], v[170:171], 0, s[14:15]
	v_readlane_b32 s14, v181, 8
	global_store_dwordx2 v[118:119], v[114:115], off
	global_store_dwordx2 v[118:119], v[116:117], off offset:512
	s_waitcnt vmcnt(31)
	v_lshlrev_b32_e32 v114, 16, v110
	v_mul_f32_e32 v118, s14, v2
	v_and_b32_e32 v110, 0xffff0000, v110
	v_mul_f32_e32 v114, v118, v114
	v_mul_f32_e32 v118, s14, v3
	v_lshlrev_b32_e32 v115, 16, v111
	v_mul_f32_e32 v110, v118, v110
	v_mul_f32_e32 v118, s14, v4
	v_and_b32_e32 v111, 0xffff0000, v111
	v_mul_f32_e32 v115, v118, v115
	v_mul_f32_e32 v118, s14, v5
	v_lshlrev_b32_e32 v116, 16, v112
	v_mul_f32_e32 v111, v118, v111
	v_mul_f32_e32 v118, s14, v6
	v_and_b32_e32 v112, 0xffff0000, v112
	v_mul_f32_e32 v116, v118, v116
	v_mul_f32_e32 v118, s14, v7
	v_lshlrev_b32_e32 v117, 16, v113
	v_mul_f32_e32 v112, v118, v112
	v_mul_f32_e32 v118, s14, v8
	v_and_b32_e32 v113, 0xffff0000, v113
	v_mul_f32_e32 v117, v118, v117
	v_mul_f32_e32 v118, s14, v9
	v_mul_f32_e32 v113, v118, v113
	s_waitcnt vmcnt(30)
; __device__ __forceinline__ unsigned pk4_fp8(float a, float b, float c, float d) { unsigned w = 0u; w = __builtin_amdgcn_cvt_pk_fp8_f32(a, b, w, false); w = __builtin_amdgcn_cvt_pk_fp8_f32(c, d, w, true); return w; }
; __device__ __forceinline__ void unpack8(const v4u w, float (&y)[8]) { y[0] = bf_lo(w.x); y[1] = bf_hi(w.x); y[2] = bf_lo(w.y); y[3] = bf_hi(w.y); y[4] = bf_lo(w.z); y[5] = bf_hi(w.z); y[6] = bf_lo(w.w); y[7] = bf_hi(w.w); }
; __device__ __forceinline__ void norm_router_phase(const bf16* x1, const float* g, const float* Wr, unsigned char* XN8, float* AFF, LAS float* WT, int gw, int NGW, int lane, int tid, bool table_ready) {
;     ...
;         for (int i = 0; i < 16; ++i) { const bf16* xr = x1 + (size_t)(row0 + i) * DM + 8 * lane; xa[i] = *(const v4u*)xr; xb[i] = *(const v4u*)(xr + 512); }
; #pragma unroll
;         for (int i = 0; i < 16; ++i) {
;             const float rs = __uint_as_float((unsigned)__builtin_amdgcn_readlane((int)rbits, i));
;             float v[16]; { float t[8]; unpack8(xa[i], t);
; #pragma unroll
;                 for (int j = 0; j < 8; ++j) v[j] = t[j] * (rs * gg[j]);
;                 unpack8(xb[i], t);
; #pragma unroll
;                 for (int j = 0; j < 8; ++j) v[8 + j] = t[j] * (rs * gg[8 + j]); }
;             unsigned char* o = XN8 + (size_t)(row0 + i) * DM + 8 * lane;
;             *(v2u*)o = (v2u){pg8::pk4_fp8(v[0], v[1], v[2], v[3]), pg8::pk4_fp8(v[4], v[5], v[6], v[7])};
;             *(v2u*)(o + 512) = (v2u){pg8::pk4_fp8(v[8], v[9], v[10], v[11]), pg8::pk4_fp8(v[12], v[13], v[14], v[15])};
;         }
	v_lshlrev_b32_e32 v118, 16, v106
	v_mul_f32_e32 v122, s14, v10
	v_and_b32_e32 v106, 0xffff0000, v106
	v_mul_f32_e32 v118, v122, v118
	v_mul_f32_e32 v122, s14, v11
	v_lshlrev_b32_e32 v119, 16, v107
	v_mul_f32_e32 v122, v122, v106
	v_mul_f32_e32 v106, s14, v12
	v_and_b32_e32 v107, 0xffff0000, v107
	v_mul_f32_e32 v119, v106, v119
	v_mul_f32_e32 v106, s14, v13
	v_lshlrev_b32_e32 v120, 16, v108
	v_mul_f32_e32 v123, v106, v107
	v_mul_f32_e32 v106, s14, v14
	v_and_b32_e32 v108, 0xffff0000, v108
	v_mul_f32_e32 v120, v106, v120
	v_mul_f32_e32 v106, s14, v15
	v_lshlrev_b32_e32 v121, 16, v109
	v_mul_f32_e32 v124, v106, v108
	v_mul_f32_e32 v106, s14, v16
	v_and_b32_e32 v109, 0xffff0000, v109
	v_mul_f32_e32 v121, v106, v121
	v_mul_f32_e32 v106, s14, v17
	v_mul_f32_e32 v125, v106, v109
	v_mov_b32_e32 v106, v163
	v_mov_b32_e32 v107, v163
	v_cvt_pk_fp8_f32 v106, v114, v110
	v_cvt_pk_fp8_f32 v107, v116, v112
	v_mov_b32_e32 v108, v163
	v_mov_b32_e32 v109, v163
	v_cvt_pk_fp8_f32 v108, v118, v122
	v_cvt_pk_fp8_f32 v109, v120, v124
	v_cvt_pk_fp8_f32 v106, v115, v111 op_sel:[0,0,1]
	v_cvt_pk_fp8_f32 v107, v117, v113 op_sel:[0,0,1]
	v_cvt_pk_fp8_f32 v108, v119, v123 op_sel:[0,0,1]
	v_cvt_pk_fp8_f32 v109, v121, v125 op_sel:[0,0,1]
	s_lshl_b64 s[14:15], s[20:21], 10
	v_lshl_add_u64 v[110:111], v[170:171], 0, s[14:15]
	v_readlane_b32 s14, v181, 9
	global_store_dwordx2 v[110:111], v[106:107], off
	global_store_dwordx2 v[110:111], v[108:109], off offset:512
	s_waitcnt vmcnt(31)
	v_lshlrev_b32_e32 v106, 16, v102
	v_mul_f32_e32 v110, s14, v2
	v_and_b32_e32 v102, 0xffff0000, v102
	v_mul_f32_e32 v106, v110, v106
	v_mul_f32_e32 v110, s14, v3
	v_lshlrev_b32_e32 v107, 16, v103
	v_mul_f32_e32 v102, v110, v102
	v_mul_f32_e32 v110, s14, v4
	v_and_b32_e32 v103, 0xffff0000, v103
	v_mul_f32_e32 v107, v110, v107
	v_mul_f32_e32 v110, s14, v5
	v_lshlrev_b32_e32 v108, 16, v104
	v_mul_f32_e32 v103, v110, v103
	v_mul_f32_e32 v110, s14, v6
	v_and_b32_e32 v104, 0xffff0000, v104
	v_mul_f32_e32 v108, v110, v108
	v_mul_f32_e32 v110, s14, v7
	v_lshlrev_b32_e32 v109, 16, v105
	v_mul_f32_e32 v104, v110, v104
	v_mul_f32_e32 v110, s14, v8
	v_and_b32_e32 v105, 0xffff0000, v105
	v_mul_f32_e32 v109, v110, v109
	v_mul_f32_e32 v110, s14, v9
	v_mul_f32_e32 v105, v110, v105
	s_waitcnt vmcnt(30)
	v_lshlrev_b32_e32 v110, 16, v98
	v_mul_f32_e32 v114, s14, v10
	v_and_b32_e32 v98, 0xffff0000, v98
	v_mul_f32_e32 v110, v114, v110
	v_mul_f32_e32 v114, s14, v11
	v_lshlrev_b32_e32 v111, 16, v99
	v_mul_f32_e32 v114, v114, v98
	v_mul_f32_e32 v98, s14, v12
	v_and_b32_e32 v99, 0xffff0000, v99
	v_mul_f32_e32 v111, v98, v111
	v_mul_f32_e32 v98, s14, v13
	v_lshlrev_b32_e32 v112, 16, v100
	v_mul_f32_e32 v115, v98, v99
	v_mul_f32_e32 v98, s14, v14
	v_and_b32_e32 v100, 0xffff0000, v100
	v_mul_f32_e32 v112, v98, v112
	v_mul_f32_e32 v98, s14, v15
	v_lshlrev_b32_e32 v113, 16, v101
	v_mul_f32_e32 v116, v98, v100
	v_mul_f32_e32 v98, s14, v16
	v_and_b32_e32 v101, 0xffff0000, v101
	v_mul_f32_e32 v113, v98, v113
	v_mul_f32_e32 v98, s14, v17
	v_mul_f32_e32 v117, v98, v101
	v_mov_b32_e32 v98, v163
	v_mov_b32_e32 v99, v163
	v_cvt_pk_fp8_f32 v98, v106, v102
	v_cvt_pk_fp8_f32 v99, v108, v104
	v_mov_b32_e32 v100, v163
	v_mov_b32_e32 v101, v163
	v_cvt_pk_fp8_f32 v100, v110, v114
	v_cvt_pk_fp8_f32 v101, v112, v116
	v_cvt_pk_fp8_f32 v98, v107, v103 op_sel:[0,0,1]
	v_cvt_pk_fp8_f32 v99, v109, v105 op_sel:[0,0,1]
	v_cvt_pk_fp8_f32 v100, v111, v115 op_sel:[0,0,1]
	v_cvt_pk_fp8_f32 v101, v113, v117 op_sel:[0,0,1]
	s_lshl_b64 s[14:15], s[18:19], 10
	v_lshl_add_u64 v[102:103], v[170:171], 0, s[14:15]
	v_readlane_b32 s14, v181, 10
	global_store_dwordx2 v[102:103], v[98:99], off
	global_store_dwordx2 v[102:103], v[100:101], off offset:512
	s_waitcnt vmcnt(31)
	v_lshlrev_b32_e32 v98, 16, v94
	v_mul_f32_e32 v102, s14, v2
	v_and_b32_e32 v94, 0xffff0000, v94
	v_mul_f32_e32 v98, v102, v98
	v_mul_f32_e32 v102, s14, v3
	v_lshlrev_b32_e32 v99, 16, v95
	v_mul_f32_e32 v94, v102, v94
	v_mul_f32_e32 v102, s14, v4
	v_and_b32_e32 v95, 0xffff0000, v95
	v_mul_f32_e32 v99, v102, v99
	v_mul_f32_e32 v102, s14, v5
	v_lshlrev_b32_e32 v100, 16, v96
	v_mul_f32_e32 v95, v102, v95
	v_mul_f32_e32 v102, s14, v6
	v_and_b32_e32 v96, 0xffff0000, v96
	v_mul_f32_e32 v100, v102, v100
	v_mul_f32_e32 v102, s14, v7
	v_lshlrev_b32_e32 v101, 16, v97
	v_mul_f32_e32 v96, v102, v96
	v_mul_f32_e32 v102, s14, v8
	v_and_b32_e32 v97, 0xffff0000, v97
	v_mul_f32_e32 v101, v102, v101
	v_mul_f32_e32 v102, s14, v9
	v_mul_f32_e32 v97, v102, v97
	s_waitcnt vmcnt(30)
	v_lshlrev_b32_e32 v102, 16, v90
	v_mul_f32_e32 v106, s14, v10
	v_and_b32_e32 v90, 0xffff0000, v90
	v_mul_f32_e32 v102, v106, v102
	v_mul_f32_e32 v106, s14, v11
	v_lshlrev_b32_e32 v103, 16, v91
	v_mul_f32_e32 v106, v106, v90
	v_mul_f32_e32 v90, s14, v12
	v_and_b32_e32 v91, 0xffff0000, v91
	v_mul_f32_e32 v103, v90, v103
	v_mul_f32_e32 v90, s14, v13
	v_lshlrev_b32_e32 v104, 16, v92
	v_mul_f32_e32 v107, v90, v91
	v_mul_f32_e32 v90, s14, v14
	v_and_b32_e32 v92, 0xffff0000, v92
	v_mul_f32_e32 v104, v90, v104
	v_mul_f32_e32 v90, s14, v15
	v_lshlrev_b32_e32 v105, 16, v93
	v_mul_f32_e32 v108, v90, v92
	v_mul_f32_e32 v90, s14, v16
	v_and_b32_e32 v93, 0xffff0000, v93
	v_mul_f32_e32 v105, v90, v105
	v_mul_f32_e32 v90, s14, v17
	v_mul_f32_e32 v109, v90, v93
	v_mov_b32_e32 v90, v163
	v_mov_b32_e32 v91, v163
	v_cvt_pk_fp8_f32 v90, v98, v94
	v_cvt_pk_fp8_f32 v91, v100, v96
	v_mov_b32_e32 v92, v163
	v_mov_b32_e32 v93, v163
	v_cvt_pk_fp8_f32 v92, v102, v106
	v_cvt_pk_fp8_f32 v93, v104, v108
	v_cvt_pk_fp8_f32 v90, v99, v95 op_sel:[0,0,1]
	v_cvt_pk_fp8_f32 v91, v101, v97 op_sel:[0,0,1]
	v_cvt_pk_fp8_f32 v92, v103, v107 op_sel:[0,0,1]
	v_cvt_pk_fp8_f32 v93, v105, v109 op_sel:[0,0,1]
	s_lshl_b64 s[14:15], s[16:17], 10
	v_lshl_add_u64 v[94:95], v[170:171], 0, s[14:15]
	v_readlane_b32 s14, v181, 11
	global_store_dwordx2 v[94:95], v[90:91], off
	global_store_dwordx2 v[94:95], v[92:93], off offset:512
	s_waitcnt vmcnt(31)
; __device__ __forceinline__ unsigned pk4_fp8(float a, float b, float c, float d) { unsigned w = 0u; w = __builtin_amdgcn_cvt_pk_fp8_f32(a, b, w, false); w = __builtin_amdgcn_cvt_pk_fp8_f32(c, d, w, true); return w; }
; __device__ __forceinline__ void unpack8(const v4u w, float (&y)[8]) { y[0] = bf_lo(w.x); y[1] = bf_hi(w.x); y[2] = bf_lo(w.y); y[3] = bf_hi(w.y); y[4] = bf_lo(w.z); y[5] = bf_hi(w.z); y[6] = bf_lo(w.w); y[7] = bf_hi(w.w); }
; __device__ __forceinline__ void norm_router_phase(const bf16* x1, const float* g, const float* Wr, unsigned char* XN8, float* AFF, LAS float* WT, int gw, int NGW, int lane, int tid, bool table_ready) {
;     ...
;         for (int i = 0; i < 16; ++i) { const bf16* xr = x1 + (size_t)(row0 + i) * DM + 8 * lane; xa[i] = *(const v4u*)xr; xb[i] = *(const v4u*)(xr + 512); }
; #pragma unroll
;         for (int i = 0; i < 16; ++i) {
;             const float rs = __uint_as_float((unsigned)__builtin_amdgcn_readlane((int)rbits, i));
;             float v[16]; { float t[8]; unpack8(xa[i], t);
; #pragma unroll
;                 for (int j = 0; j < 8; ++j) v[j] = t[j] * (rs * gg[j]);
;                 unpack8(xb[i], t);
; #pragma unroll
;                 for (int j = 0; j < 8; ++j) v[8 + j] = t[j] * (rs * gg[8 + j]); }
;             unsigned char* o = XN8 + (size_t)(row0 + i) * DM + 8 * lane;
;             *(v2u*)o = (v2u){pg8::pk4_fp8(v[0], v[1], v[2], v[3]), pg8::pk4_fp8(v[4], v[5], v[6], v[7])};
;             *(v2u*)(o + 512) = (v2u){pg8::pk4_fp8(v[8], v[9], v[10], v[11]), pg8::pk4_fp8(v[12], v[13], v[14], v[15])};
;         }
	v_lshlrev_b32_e32 v90, 16, v86
	v_mul_f32_e32 v94, s14, v2
	v_and_b32_e32 v86, 0xffff0000, v86
	v_mul_f32_e32 v90, v94, v90
	v_mul_f32_e32 v94, s14, v3
	v_lshlrev_b32_e32 v91, 16, v87
	v_mul_f32_e32 v86, v94, v86
	v_mul_f32_e32 v94, s14, v4
	v_and_b32_e32 v87, 0xffff0000, v87
	v_mul_f32_e32 v91, v94, v91
	v_mul_f32_e32 v94, s14, v5
	v_lshlrev_b32_e32 v92, 16, v88
	v_mul_f32_e32 v87, v94, v87
	v_mul_f32_e32 v94, s14, v6
	v_and_b32_e32 v88, 0xffff0000, v88
	v_mul_f32_e32 v92, v94, v92
	v_mul_f32_e32 v94, s14, v7
	v_lshlrev_b32_e32 v93, 16, v89
	v_mul_f32_e32 v88, v94, v88
	v_mul_f32_e32 v94, s14, v8
	v_and_b32_e32 v89, 0xffff0000, v89
	v_mul_f32_e32 v93, v94, v93
	v_mul_f32_e32 v94, s14, v9
	v_mul_f32_e32 v89, v94, v89
	s_waitcnt vmcnt(30)
	v_lshlrev_b32_e32 v94, 16, v82
	v_mul_f32_e32 v98, s14, v10
	v_and_b32_e32 v82, 0xffff0000, v82
	v_mul_f32_e32 v94, v98, v94
	v_mul_f32_e32 v98, s14, v11
	v_lshlrev_b32_e32 v95, 16, v83
	v_mul_f32_e32 v98, v98, v82
	v_mul_f32_e32 v82, s14, v12
	v_and_b32_e32 v83, 0xffff0000, v83
	v_mul_f32_e32 v95, v82, v95
	v_mul_f32_e32 v82, s14, v13
	v_lshlrev_b32_e32 v96, 16, v84
	v_mul_f32_e32 v99, v82, v83
	v_mul_f32_e32 v82, s14, v14
	v_and_b32_e32 v84, 0xffff0000, v84
	v_mul_f32_e32 v96, v82, v96
	v_mul_f32_e32 v82, s14, v15
	v_lshlrev_b32_e32 v97, 16, v85
	v_mul_f32_e32 v100, v82, v84
	v_mul_f32_e32 v82, s14, v16
	v_and_b32_e32 v85, 0xffff0000, v85
	v_mul_f32_e32 v97, v82, v97
	v_mul_f32_e32 v82, s14, v17
	v_mul_f32_e32 v101, v82, v85
	v_mov_b32_e32 v82, v163
	v_mov_b32_e32 v83, v163
	v_cvt_pk_fp8_f32 v82, v90, v86
	v_cvt_pk_fp8_f32 v83, v92, v88
	v_mov_b32_e32 v84, v163
	v_mov_b32_e32 v85, v163
	v_cvt_pk_fp8_f32 v84, v94, v98
	v_cvt_pk_fp8_f32 v85, v96, v100
	v_cvt_pk_fp8_f32 v82, v91, v87 op_sel:[0,0,1]
	v_cvt_pk_fp8_f32 v83, v93, v89 op_sel:[0,0,1]
	v_cvt_pk_fp8_f32 v84, v95, v99 op_sel:[0,0,1]
	v_cvt_pk_fp8_f32 v85, v97, v101 op_sel:[0,0,1]
	v_lshl_add_u64 v[86:87], v[170:171], 0, s[12:13]
	v_readlane_b32 s12, v181, 12
	global_store_dwordx2 v[86:87], v[82:83], off
	global_store_dwordx2 v[86:87], v[84:85], off offset:512
	s_waitcnt vmcnt(31)
	v_lshlrev_b32_e32 v82, 16, v78
	v_mul_f32_e32 v86, s12, v2
	v_and_b32_e32 v78, 0xffff0000, v78
	v_mul_f32_e32 v82, v86, v82
	v_mul_f32_e32 v86, s12, v3
	v_lshlrev_b32_e32 v83, 16, v79
	v_mul_f32_e32 v78, v86, v78
	v_mul_f32_e32 v86, s12, v4
	v_and_b32_e32 v79, 0xffff0000, v79
	v_mul_f32_e32 v83, v86, v83
	v_mul_f32_e32 v86, s12, v5
	v_lshlrev_b32_e32 v84, 16, v80
	v_mul_f32_e32 v79, v86, v79
	v_mul_f32_e32 v86, s12, v6
	v_and_b32_e32 v80, 0xffff0000, v80
	v_mul_f32_e32 v84, v86, v84
	v_mul_f32_e32 v86, s12, v7
	v_lshlrev_b32_e32 v85, 16, v81
	v_mul_f32_e32 v80, v86, v80
	v_mul_f32_e32 v86, s12, v8
	v_and_b32_e32 v81, 0xffff0000, v81
	v_mul_f32_e32 v85, v86, v85
	v_mul_f32_e32 v86, s12, v9
	v_mul_f32_e32 v81, v86, v81
	s_waitcnt vmcnt(30)
	v_lshlrev_b32_e32 v86, 16, v74
	v_mul_f32_e32 v90, s12, v10
	v_and_b32_e32 v74, 0xffff0000, v74
	v_mul_f32_e32 v86, v90, v86
	v_mul_f32_e32 v90, s12, v11
	v_lshlrev_b32_e32 v87, 16, v75
	v_mul_f32_e32 v90, v90, v74
	v_mul_f32_e32 v74, s12, v12
	v_and_b32_e32 v75, 0xffff0000, v75
	v_mul_f32_e32 v87, v74, v87
	v_mul_f32_e32 v74, s12, v13
	v_lshlrev_b32_e32 v88, 16, v76
	v_mul_f32_e32 v91, v74, v75
	v_mul_f32_e32 v74, s12, v14
	v_and_b32_e32 v76, 0xffff0000, v76
	v_mul_f32_e32 v88, v74, v88
	v_mul_f32_e32 v74, s12, v15
	v_lshlrev_b32_e32 v89, 16, v77
	v_mul_f32_e32 v92, v74, v76
	v_mul_f32_e32 v74, s12, v16
	v_and_b32_e32 v77, 0xffff0000, v77
	v_mul_f32_e32 v89, v74, v89
	v_mul_f32_e32 v74, s12, v17
	v_mul_f32_e32 v93, v74, v77
	v_mov_b32_e32 v74, v163
	v_mov_b32_e32 v75, v163
	v_cvt_pk_fp8_f32 v74, v82, v78
	v_cvt_pk_fp8_f32 v75, v84, v80
	v_mov_b32_e32 v76, v163
	v_mov_b32_e32 v77, v163
	v_cvt_pk_fp8_f32 v76, v86, v90
	v_cvt_pk_fp8_f32 v77, v88, v92
	v_cvt_pk_fp8_f32 v74, v83, v79 op_sel:[0,0,1]
	v_cvt_pk_fp8_f32 v75, v85, v81 op_sel:[0,0,1]
	v_cvt_pk_fp8_f32 v76, v87, v91 op_sel:[0,0,1]
	v_cvt_pk_fp8_f32 v77, v89, v93 op_sel:[0,0,1]
	v_lshl_add_u64 v[78:79], v[170:171], 0, s[10:11]
	v_readlane_b32 s10, v181, 13
	global_store_dwordx2 v[78:79], v[74:75], off
	global_store_dwordx2 v[78:79], v[76:77], off offset:512
	s_waitcnt vmcnt(31)
	v_lshlrev_b32_e32 v74, 16, v70
	v_mul_f32_e32 v78, s10, v2
	v_and_b32_e32 v70, 0xffff0000, v70
	v_mul_f32_e32 v74, v78, v74
	v_mul_f32_e32 v78, s10, v3
	v_lshlrev_b32_e32 v75, 16, v71
	v_mul_f32_e32 v70, v78, v70
	v_mul_f32_e32 v78, s10, v4
	v_and_b32_e32 v71, 0xffff0000, v71
	v_mul_f32_e32 v75, v78, v75
	v_mul_f32_e32 v78, s10, v5
	v_lshlrev_b32_e32 v76, 16, v72
	v_mul_f32_e32 v71, v78, v71
	v_mul_f32_e32 v78, s10, v6
	v_and_b32_e32 v72, 0xffff0000, v72
	v_mul_f32_e32 v76, v78, v76
	v_mul_f32_e32 v78, s10, v7
	v_lshlrev_b32_e32 v77, 16, v73
	v_mul_f32_e32 v72, v78, v72
	v_mul_f32_e32 v78, s10, v8
	v_and_b32_e32 v73, 0xffff0000, v73
	v_mul_f32_e32 v77, v78, v77
	v_mul_f32_e32 v78, s10, v9
	v_mul_f32_e32 v73, v78, v73
	s_waitcnt vmcnt(30)
; __device__ __forceinline__ unsigned pk4_fp8(float a, float b, float c, float d) { unsigned w = 0u; w = __builtin_amdgcn_cvt_pk_fp8_f32(a, b, w, false); w = __builtin_amdgcn_cvt_pk_fp8_f32(c, d, w, true); return w; }
; __device__ __forceinline__ void unpack8(const v4u w, float (&y)[8]) { y[0] = bf_lo(w.x); y[1] = bf_hi(w.x); y[2] = bf_lo(w.y); y[3] = bf_hi(w.y); y[4] = bf_lo(w.z); y[5] = bf_hi(w.z); y[6] = bf_lo(w.w); y[7] = bf_hi(w.w); }
; __device__ __forceinline__ void norm_router_phase(const bf16* x1, const float* g, const float* Wr, unsigned char* XN8, float* AFF, LAS float* WT, int gw, int NGW, int lane, int tid, bool table_ready) {
;     ...
;     for (int grp = gw; grp < NTOK / 16; grp += NGW) {
;     ...
;         for (int i = 0; i < 16; ++i) { const bf16* xr = x1 + (size_t)(row0 + i) * DM + 8 * lane; xa[i] = *(const v4u*)xr; xb[i] = *(const v4u*)(xr + 512); }
; #pragma unroll
;         for (int i = 0; i < 16; ++i) {
;             const float rs = __uint_as_float((unsigned)__builtin_amdgcn_readlane((int)rbits, i));
;             float v[16]; { float t[8]; unpack8(xa[i], t);
; #pragma unroll
;                 for (int j = 0; j < 8; ++j) v[j] = t[j] * (rs * gg[j]);
;                 unpack8(xb[i], t);
; #pragma unroll
;                 for (int j = 0; j < 8; ++j) v[8 + j] = t[j] * (rs * gg[8 + j]); }
;             unsigned char* o = XN8 + (size_t)(row0 + i) * DM + 8 * lane;
;             *(v2u*)o = (v2u){pg8::pk4_fp8(v[0], v[1], v[2], v[3]), pg8::pk4_fp8(v[4], v[5], v[6], v[7])};
;             *(v2u*)(o + 512) = (v2u){pg8::pk4_fp8(v[8], v[9], v[10], v[11]), pg8::pk4_fp8(v[12], v[13], v[14], v[15])};
;         }
	v_lshlrev_b32_e32 v78, 16, v66
	v_mul_f32_e32 v82, s10, v10
	v_and_b32_e32 v66, 0xffff0000, v66
	v_mul_f32_e32 v78, v82, v78
	v_mul_f32_e32 v82, s10, v11
	v_lshlrev_b32_e32 v79, 16, v67
	v_mul_f32_e32 v82, v82, v66
	v_mul_f32_e32 v66, s10, v12
	v_and_b32_e32 v67, 0xffff0000, v67
	v_mul_f32_e32 v79, v66, v79
	v_mul_f32_e32 v66, s10, v13
	v_lshlrev_b32_e32 v80, 16, v68
	v_mul_f32_e32 v83, v66, v67
	v_mul_f32_e32 v66, s10, v14
	v_and_b32_e32 v68, 0xffff0000, v68
	v_mul_f32_e32 v80, v66, v80
	v_mul_f32_e32 v66, s10, v15
	v_lshlrev_b32_e32 v81, 16, v69
	v_mul_f32_e32 v84, v66, v68
	v_mul_f32_e32 v66, s10, v16
	v_and_b32_e32 v69, 0xffff0000, v69
	v_mul_f32_e32 v81, v66, v81
	v_mul_f32_e32 v66, s10, v17
	v_mul_f32_e32 v85, v66, v69
	v_mov_b32_e32 v66, v163
	v_mov_b32_e32 v67, v163
	v_cvt_pk_fp8_f32 v66, v74, v70
	v_cvt_pk_fp8_f32 v67, v76, v72
	v_mov_b32_e32 v68, v163
	v_mov_b32_e32 v69, v163
	v_cvt_pk_fp8_f32 v68, v78, v82
	v_cvt_pk_fp8_f32 v69, v80, v84
	v_cvt_pk_fp8_f32 v66, v75, v71 op_sel:[0,0,1]
	v_cvt_pk_fp8_f32 v67, v77, v73 op_sel:[0,0,1]
	v_cvt_pk_fp8_f32 v68, v79, v83 op_sel:[0,0,1]
	v_cvt_pk_fp8_f32 v69, v81, v85 op_sel:[0,0,1]
	v_lshl_add_u64 v[70:71], v[170:171], 0, s[8:9]
	v_readlane_b32 s8, v181, 14
	global_store_dwordx2 v[70:71], v[66:67], off
	global_store_dwordx2 v[70:71], v[68:69], off offset:512
	s_waitcnt vmcnt(31)
	v_lshlrev_b32_e32 v66, 16, v62
	v_mul_f32_e32 v70, s8, v2
	v_and_b32_e32 v62, 0xffff0000, v62
	v_mul_f32_e32 v66, v70, v66
	v_mul_f32_e32 v70, s8, v3
	v_lshlrev_b32_e32 v67, 16, v63
	v_mul_f32_e32 v62, v70, v62
	v_mul_f32_e32 v70, s8, v4
	v_and_b32_e32 v63, 0xffff0000, v63
	v_mul_f32_e32 v67, v70, v67
	v_mul_f32_e32 v70, s8, v5
	v_lshlrev_b32_e32 v68, 16, v64
	v_mul_f32_e32 v63, v70, v63
	v_mul_f32_e32 v70, s8, v6
	v_and_b32_e32 v64, 0xffff0000, v64
	v_mul_f32_e32 v68, v70, v68
	v_mul_f32_e32 v70, s8, v7
	v_lshlrev_b32_e32 v69, 16, v65
	v_mul_f32_e32 v64, v70, v64
	v_mul_f32_e32 v70, s8, v8
	v_and_b32_e32 v65, 0xffff0000, v65
	v_mul_f32_e32 v69, v70, v69
	v_mul_f32_e32 v70, s8, v9
	v_mul_f32_e32 v65, v70, v65
	s_waitcnt vmcnt(30)
	v_lshlrev_b32_e32 v70, 16, v58
	v_mul_f32_e32 v74, s8, v10
	v_and_b32_e32 v58, 0xffff0000, v58
	v_mul_f32_e32 v70, v74, v70
	v_mul_f32_e32 v74, s8, v11
	v_lshlrev_b32_e32 v71, 16, v59
	v_mul_f32_e32 v74, v74, v58
	v_mul_f32_e32 v58, s8, v12
	v_and_b32_e32 v59, 0xffff0000, v59
	v_mul_f32_e32 v71, v58, v71
	v_mul_f32_e32 v58, s8, v13
	v_lshlrev_b32_e32 v72, 16, v60
	v_mul_f32_e32 v75, v58, v59
	v_mul_f32_e32 v58, s8, v14
	v_and_b32_e32 v60, 0xffff0000, v60
	v_mul_f32_e32 v72, v58, v72
	v_mul_f32_e32 v58, s8, v15
	v_lshlrev_b32_e32 v73, 16, v61
	v_mul_f32_e32 v76, v58, v60
	v_mul_f32_e32 v58, s8, v16
	v_and_b32_e32 v61, 0xffff0000, v61
	v_mul_f32_e32 v73, v58, v73
	v_mul_f32_e32 v58, s8, v17
	v_mul_f32_e32 v77, v58, v61
	v_mov_b32_e32 v58, v163
	v_mov_b32_e32 v59, v163
	v_cvt_pk_fp8_f32 v58, v66, v62
	v_cvt_pk_fp8_f32 v59, v68, v64
	v_mov_b32_e32 v60, v163
	v_mov_b32_e32 v61, v163
	v_cvt_pk_fp8_f32 v60, v70, v74
	v_cvt_pk_fp8_f32 v61, v72, v76
	v_cvt_pk_fp8_f32 v58, v67, v63 op_sel:[0,0,1]
	v_cvt_pk_fp8_f32 v59, v69, v65 op_sel:[0,0,1]
	v_cvt_pk_fp8_f32 v60, v71, v75 op_sel:[0,0,1]
	v_cvt_pk_fp8_f32 v61, v73, v77 op_sel:[0,0,1]
	v_lshl_add_u64 v[62:63], v[170:171], 0, s[4:5]
	v_readlane_b32 s4, v181, 15
	global_store_dwordx2 v[62:63], v[58:59], off
	global_store_dwordx2 v[62:63], v[60:61], off offset:512
	s_waitcnt vmcnt(31)
	v_lshlrev_b32_e32 v58, 16, v54
	v_mul_f32_e32 v62, s4, v2
	v_and_b32_e32 v54, 0xffff0000, v54
	v_mul_f32_e32 v58, v62, v58
	v_mul_f32_e32 v62, s4, v3
	v_lshlrev_b32_e32 v59, 16, v55
	v_mul_f32_e32 v54, v62, v54
	v_mul_f32_e32 v62, s4, v4
	v_and_b32_e32 v55, 0xffff0000, v55
	v_mul_f32_e32 v59, v62, v59
	v_mul_f32_e32 v62, s4, v5
	v_lshlrev_b32_e32 v60, 16, v56
	v_mul_f32_e32 v55, v62, v55
	v_mul_f32_e32 v62, s4, v6
	v_and_b32_e32 v56, 0xffff0000, v56
	v_mul_f32_e32 v60, v62, v60
	v_mul_f32_e32 v62, s4, v7
	v_lshlrev_b32_e32 v61, 16, v57
	v_mul_f32_e32 v56, v62, v56
	v_mul_f32_e32 v62, s4, v8
	v_and_b32_e32 v57, 0xffff0000, v57
	v_mul_f32_e32 v61, v62, v61
	v_mul_f32_e32 v62, s4, v9
	v_mul_f32_e32 v57, v62, v57
	s_waitcnt vmcnt(30)
	v_lshlrev_b32_e32 v62, 16, v50
	v_mul_f32_e32 v66, s4, v10
	v_and_b32_e32 v50, 0xffff0000, v50
	v_mul_f32_e32 v62, v66, v62
	v_mul_f32_e32 v66, s4, v11
	v_lshlrev_b32_e32 v63, 16, v51
	v_mul_f32_e32 v66, v66, v50
	v_mul_f32_e32 v50, s4, v12
	v_and_b32_e32 v51, 0xffff0000, v51
	v_mul_f32_e32 v63, v50, v63
	v_mul_f32_e32 v50, s4, v13
	v_lshlrev_b32_e32 v64, 16, v52
	v_mul_f32_e32 v67, v50, v51
	v_mul_f32_e32 v50, s4, v14
	v_and_b32_e32 v52, 0xffff0000, v52
	v_mul_f32_e32 v64, v50, v64
	v_mul_f32_e32 v50, s4, v15
	v_lshlrev_b32_e32 v65, 16, v53
	v_mul_f32_e32 v68, v50, v52
	v_mul_f32_e32 v50, s4, v16
	v_and_b32_e32 v53, 0xffff0000, v53
	v_mul_f32_e32 v65, v50, v65
	v_mul_f32_e32 v50, s4, v17
	v_mul_f32_e32 v69, v50, v53
	v_mov_b32_e32 v50, v163
	v_mov_b32_e32 v51, v163
	v_cvt_pk_fp8_f32 v50, v58, v54
	v_cvt_pk_fp8_f32 v51, v60, v56
	v_mov_b32_e32 v52, v163
	v_mov_b32_e32 v53, v163
	v_cvt_pk_fp8_f32 v52, v62, v66
	v_cvt_pk_fp8_f32 v53, v64, v68
	v_cvt_pk_fp8_f32 v50, v59, v55 op_sel:[0,0,1]
	v_cvt_pk_fp8_f32 v51, v61, v57 op_sel:[0,0,1]
	v_cvt_pk_fp8_f32 v52, v63, v67 op_sel:[0,0,1]
	v_cvt_pk_fp8_f32 v53, v65, v69 op_sel:[0,0,1]
	v_lshl_add_u64 v[54:55], v[170:171], 0, s[2:3]
	v_readlane_b32 s2, v254, 52
	s_add_i32 s40, s40, s2
	s_cmpk_gt_i32 s40, 0x7ff
	global_store_dwordx2 v[54:55], v[50:51], off
	global_store_dwordx2 v[54:55], v[52:53], off offset:512
	s_cbranch_scc1 .LBB0_1281
